# GEMM k-loops: the already-satisfied lgkmcnt(0) between each barrier release and the first MFMA of the segment removed (the pre-barrier lgkmcnt(0) covers it)
# speedup vs baseline: 1.0038x; 1.0021x over previous
.Lprio_P2a:
.LBB0_418:
	ds_read_b128 v[148:151], v168
	ds_read_b128 v[152:155], v168 offset:1024
	ds_read_b128 v[172:175], v168 offset:2048
	ds_read_b128 v[176:179], v168 offset:3072
	ds_read_b128 v[186:189], v169
	ds_read_b128 v[190:193], v169 offset:1024
	ds_read_b128 v[194:197], v169 offset:2048
	ds_read_b128 v[198:201], v169 offset:3072
	s_add_u32 s38, s34, 0xfff00080
	s_addc_u32 s39, s35, -1
	s_cmp_eq_u32 s67, 60
	s_cselect_b32 s45, s5, s39
	s_cselect_b32 s44, s7, s38
	s_cselect_b32 s43, s15, s66
	s_cselect_b32 s42, s25, s63
	s_add_i32 m0, s46, 0xc000
	ds_read_b128 v[202:205], v170
	ds_read_b128 v[206:209], v170 offset:1024
	ds_read_b128 v[210:213], v170 offset:2048
	ds_read_b128 v[214:217], v170 offset:3072
	ds_read_b128 v[218:221], v170 offset:4096
	ds_read_b128 v[222:225], v170 offset:5120
	ds_read_b128 v[226:229], v170 offset:6144
	ds_read_b128 v[230:233], v170 offset:7168
	global_load_lds_dwordx4 v140, s[34:35]
	s_add_i32 m0, s46, 0xe000
	s_nop 0
	global_load_lds_dwordx4 v142, s[34:35]
	s_waitcnt vmcnt(8)
	s_waitcnt lgkmcnt(0)
	s_barrier
	v_mfma_f32_16x16x32_f16 v[126:129], v[148:151], v[202:205], v[126:129]
	v_mfma_f32_16x16x32_f16 v[122:125], v[172:175], v[202:205], v[122:125]
	v_mfma_f32_16x16x32_f16 v[110:113], v[148:151], v[210:213], v[110:113]
	v_mfma_f32_16x16x32_f16 v[106:109], v[172:175], v[210:213], v[106:109]
	v_mfma_f32_16x16x32_f16 v[94:97], v[148:151], v[218:221], v[94:97]
	v_mfma_f32_16x16x32_f16 v[90:93], v[172:175], v[218:221], v[90:93]
	v_mfma_f32_16x16x32_f16 v[78:81], v[148:151], v[226:229], v[78:81]
	v_mfma_f32_16x16x32_f16 v[74:77], v[172:175], v[226:229], v[74:77]
	v_mfma_f32_16x16x32_f16 v[126:129], v[152:155], v[206:209], v[126:129]
	v_mfma_f32_16x16x32_f16 v[122:125], v[176:179], v[206:209], v[122:125]
	v_mfma_f32_16x16x32_f16 v[110:113], v[152:155], v[214:217], v[110:113]
	v_mfma_f32_16x16x32_f16 v[106:109], v[176:179], v[214:217], v[106:109]
	v_mfma_f32_16x16x32_f16 v[94:97], v[152:155], v[222:225], v[94:97]
	v_mfma_f32_16x16x32_f16 v[90:93], v[176:179], v[222:225], v[90:93]
	v_mfma_f32_16x16x32_f16 v[78:81], v[152:155], v[230:233], v[78:81]
	v_mfma_f32_16x16x32_f16 v[74:77], v[176:179], v[230:233], v[74:77]
	v_mfma_f32_16x16x32_f16 v[118:121], v[186:189], v[202:205], v[118:121]
	v_mfma_f32_16x16x32_f16 v[114:117], v[194:197], v[202:205], v[114:117]
	v_mfma_f32_16x16x32_f16 v[102:105], v[186:189], v[210:213], v[102:105]
	v_mfma_f32_16x16x32_f16 v[98:101], v[194:197], v[210:213], v[98:101]
	v_mfma_f32_16x16x32_f16 v[86:89], v[186:189], v[218:221], v[86:89]
	v_mfma_f32_16x16x32_f16 v[82:85], v[194:197], v[218:221], v[82:85]
	v_mfma_f32_16x16x32_f16 v[70:73], v[186:189], v[226:229], v[70:73]
	v_mfma_f32_16x16x32_f16 v[66:69], v[194:197], v[226:229], v[66:69]
	v_mfma_f32_16x16x32_f16 v[118:121], v[190:193], v[206:209], v[118:121]
	v_mfma_f32_16x16x32_f16 v[114:117], v[198:201], v[206:209], v[114:117]
	v_mfma_f32_16x16x32_f16 v[102:105], v[190:193], v[214:217], v[102:105]
	v_mfma_f32_16x16x32_f16 v[98:101], v[198:201], v[214:217], v[98:101]
	v_mfma_f32_16x16x32_f16 v[86:89], v[190:193], v[222:225], v[86:89]
	v_mfma_f32_16x16x32_f16 v[82:85], v[198:201], v[222:225], v[82:85]
	v_mfma_f32_16x16x32_f16 v[70:73], v[190:193], v[230:233], v[70:73]
	v_mfma_f32_16x16x32_f16 v[66:69], v[198:201], v[230:233], v[66:69]
	s_barrier
	s_add_u32 s98, s42, s10
	s_addc_u32 s99, s43, s11
	s_add_u32 s100, s44, s10
	s_addc_u32 s101, s45, s11
	s_add_i32 s38, s61, s33
	s_mov_b32 m0, s38
	ds_read_b128 v[202:205], v170 offset:16384
	ds_read_b128 v[206:209], v170 offset:17408
	ds_read_b128 v[210:213], v170 offset:18432
	ds_read_b128 v[214:217], v170 offset:19456
	ds_read_b128 v[218:221], v170 offset:20480
	ds_read_b128 v[222:225], v170 offset:21504
	ds_read_b128 v[226:229], v170 offset:22528
	ds_read_b128 v[230:233], v170 offset:23552
	global_load_lds_dwordx4 v132, s[42:43]
	s_add_i32 m0, s38, 0x2000
	s_add_u32 s72, s42, 0x100000
	s_addc_u32 s73, s43, 0
	s_add_i32 s38, s62, s33
	global_load_lds_dwordx4 v136, s[42:43]
	s_mov_b32 m0, s38
	s_nop 0
	global_load_lds_dwordx4 v132, s[72:73]
	s_add_i32 m0, s38, 0x2000
	s_nop 0
	global_load_lds_dwordx4 v136, s[72:73]
	s_mov_b32 m0, s46
	s_nop 0
	global_load_lds_dwordx4 v130, s[44:45]
	s_mov_b32 m0, s47
	s_nop 0
	global_load_lds_dwordx4 v134, s[44:45]
	s_waitcnt vmcnt(8)
	s_waitcnt lgkmcnt(0)
	s_barrier
	v_mfma_f32_16x16x32_f16 v[62:65], v[148:151], v[202:205], v[62:65]
	v_mfma_f32_16x16x32_f16 v[58:61], v[172:175], v[202:205], v[58:61]
	v_mfma_f32_16x16x32_f16 v[46:49], v[148:151], v[210:213], v[46:49]
	v_mfma_f32_16x16x32_f16 v[42:45], v[172:175], v[210:213], v[42:45]
	v_mfma_f32_16x16x32_f16 v[30:33], v[148:151], v[218:221], v[30:33]
	v_mfma_f32_16x16x32_f16 v[26:29], v[172:175], v[218:221], v[26:29]
	v_mfma_f32_16x16x32_f16 v[14:17], v[148:151], v[226:229], v[14:17]
	v_mfma_f32_16x16x32_f16 v[10:13], v[172:175], v[226:229], v[10:13]
	v_mfma_f32_16x16x32_f16 v[62:65], v[152:155], v[206:209], v[62:65]
	v_mfma_f32_16x16x32_f16 v[58:61], v[176:179], v[206:209], v[58:61]
	v_mfma_f32_16x16x32_f16 v[46:49], v[152:155], v[214:217], v[46:49]
	v_mfma_f32_16x16x32_f16 v[42:45], v[176:179], v[214:217], v[42:45]
	v_mfma_f32_16x16x32_f16 v[30:33], v[152:155], v[222:225], v[30:33]
	v_mfma_f32_16x16x32_f16 v[26:29], v[176:179], v[222:225], v[26:29]
	v_mfma_f32_16x16x32_f16 v[14:17], v[152:155], v[230:233], v[14:17]
	v_mfma_f32_16x16x32_f16 v[10:13], v[176:179], v[230:233], v[10:13]
	v_mfma_f32_16x16x32_f16 v[54:57], v[186:189], v[202:205], v[54:57]
	v_mfma_f32_16x16x32_f16 v[50:53], v[194:197], v[202:205], v[50:53]
	v_mfma_f32_16x16x32_f16 v[38:41], v[186:189], v[210:213], v[38:41]
	v_mfma_f32_16x16x32_f16 v[34:37], v[194:197], v[210:213], v[34:37]
	v_mfma_f32_16x16x32_f16 v[22:25], v[186:189], v[218:221], v[22:25]
	v_mfma_f32_16x16x32_f16 v[18:21], v[194:197], v[218:221], v[18:21]
	v_mfma_f32_16x16x32_f16 v[6:9], v[186:189], v[226:229], v[6:9]
	v_mfma_f32_16x16x32_f16 v[2:5], v[194:197], v[226:229], v[2:5]
	v_mfma_f32_16x16x32_f16 v[54:57], v[190:193], v[206:209], v[54:57]
	v_mfma_f32_16x16x32_f16 v[50:53], v[198:201], v[206:209], v[50:53]
	v_mfma_f32_16x16x32_f16 v[38:41], v[190:193], v[214:217], v[38:41]
	v_mfma_f32_16x16x32_f16 v[34:37], v[198:201], v[214:217], v[34:37]
	v_mfma_f32_16x16x32_f16 v[22:25], v[190:193], v[222:225], v[22:25]
	v_mfma_f32_16x16x32_f16 v[18:21], v[198:201], v[222:225], v[18:21]
	v_mfma_f32_16x16x32_f16 v[6:9], v[190:193], v[230:233], v[6:9]
	v_mfma_f32_16x16x32_f16 v[2:5], v[198:201], v[230:233], v[2:5]
	s_barrier
	s_add_i32 s38, 0, 0x18000
	v_add_u32_e32 v138, s38, v164
	s_add_i32 s39, 0, 0x1c000
	ds_read_b128 v[148:151], v138
	ds_read_b128 v[152:155], v138 offset:1024
	ds_read_b128 v[172:175], v138 offset:2048
	ds_read_b128 v[176:179], v138 offset:3072
	v_add_u32_e32 v138, s39, v164
	ds_read_b128 v[186:189], v138
	ds_read_b128 v[190:193], v138 offset:1024
	ds_read_b128 v[194:197], v138 offset:2048
	ds_read_b128 v[198:201], v138 offset:3072
	s_add_u32 s44, s44, 0x100000
	s_addc_u32 s45, s45, 0
	s_mov_b32 m0, s50
	ds_read_b128 v[202:205], v170 offset:32768
	ds_read_b128 v[206:209], v170 offset:33792
	ds_read_b128 v[210:213], v170 offset:34816
	ds_read_b128 v[214:217], v170 offset:35840
	ds_read_b128 v[218:221], v170 offset:36864
	ds_read_b128 v[222:225], v170 offset:37888
	ds_read_b128 v[226:229], v170 offset:38912
	ds_read_b128 v[230:233], v170 offset:39936
	global_load_lds_dwordx4 v130, s[44:45]
	s_mov_b32 m0, s51
	s_nop 0
	global_load_lds_dwordx4 v134, s[44:45]
	s_waitcnt vmcnt(8)
	s_waitcnt lgkmcnt(0)
	s_barrier
	v_mfma_f32_16x16x32_f16 v[126:129], v[148:151], v[202:205], v[126:129]
	v_mfma_f32_16x16x32_f16 v[122:125], v[172:175], v[202:205], v[122:125]
	v_mfma_f32_16x16x32_f16 v[110:113], v[148:151], v[210:213], v[110:113]
	v_mfma_f32_16x16x32_f16 v[106:109], v[172:175], v[210:213], v[106:109]
	v_mfma_f32_16x16x32_f16 v[94:97], v[148:151], v[218:221], v[94:97]
	v_mfma_f32_16x16x32_f16 v[90:93], v[172:175], v[218:221], v[90:93]
	v_mfma_f32_16x16x32_f16 v[78:81], v[148:151], v[226:229], v[78:81]
	v_mfma_f32_16x16x32_f16 v[74:77], v[172:175], v[226:229], v[74:77]
	v_mfma_f32_16x16x32_f16 v[126:129], v[152:155], v[206:209], v[126:129]
	v_mfma_f32_16x16x32_f16 v[122:125], v[176:179], v[206:209], v[122:125]
	v_mfma_f32_16x16x32_f16 v[110:113], v[152:155], v[214:217], v[110:113]
	v_mfma_f32_16x16x32_f16 v[106:109], v[176:179], v[214:217], v[106:109]
	v_mfma_f32_16x16x32_f16 v[94:97], v[152:155], v[222:225], v[94:97]
	v_mfma_f32_16x16x32_f16 v[90:93], v[176:179], v[222:225], v[90:93]
	v_mfma_f32_16x16x32_f16 v[78:81], v[152:155], v[230:233], v[78:81]
	v_mfma_f32_16x16x32_f16 v[74:77], v[176:179], v[230:233], v[74:77]
	v_mfma_f32_16x16x32_f16 v[118:121], v[186:189], v[202:205], v[118:121]
	v_mfma_f32_16x16x32_f16 v[114:117], v[194:197], v[202:205], v[114:117]
	v_mfma_f32_16x16x32_f16 v[102:105], v[186:189], v[210:213], v[102:105]
	v_mfma_f32_16x16x32_f16 v[98:101], v[194:197], v[210:213], v[98:101]
	v_mfma_f32_16x16x32_f16 v[86:89], v[186:189], v[218:221], v[86:89]
	v_mfma_f32_16x16x32_f16 v[82:85], v[194:197], v[218:221], v[82:85]
	v_mfma_f32_16x16x32_f16 v[70:73], v[186:189], v[226:229], v[70:73]
	v_mfma_f32_16x16x32_f16 v[66:69], v[194:197], v[226:229], v[66:69]
	v_mfma_f32_16x16x32_f16 v[118:121], v[190:193], v[206:209], v[118:121]
	v_mfma_f32_16x16x32_f16 v[114:117], v[198:201], v[206:209], v[114:117]
	v_mfma_f32_16x16x32_f16 v[102:105], v[190:193], v[214:217], v[102:105]
	v_mfma_f32_16x16x32_f16 v[98:101], v[198:201], v[214:217], v[98:101]
	v_mfma_f32_16x16x32_f16 v[86:89], v[190:193], v[222:225], v[86:89]
	v_mfma_f32_16x16x32_f16 v[82:85], v[198:201], v[222:225], v[82:85]
	v_mfma_f32_16x16x32_f16 v[70:73], v[190:193], v[230:233], v[70:73]
	v_mfma_f32_16x16x32_f16 v[66:69], v[198:201], v[230:233], v[66:69]
	s_barrier
	s_add_i32 s38, s38, s33
	s_mov_b32 m0, s38
	ds_read_b128 v[202:205], v170 offset:49152
	ds_read_b128 v[206:209], v170 offset:50176
	ds_read_b128 v[210:213], v170 offset:51200
	ds_read_b128 v[214:217], v170 offset:52224
	ds_read_b128 v[218:221], v170 offset:53248
	ds_read_b128 v[222:225], v170 offset:54272
	ds_read_b128 v[226:229], v170 offset:55296
	ds_read_b128 v[230:233], v170 offset:56320
	global_load_lds_dwordx4 v132, s[98:99]
	s_add_i32 m0, s38, 0x2000
	s_add_u32 s42, s42, 0x100080
	s_addc_u32 s43, s43, 0
	s_add_i32 s38, s39, s33
	global_load_lds_dwordx4 v136, s[98:99]
	s_mov_b32 m0, s38
	s_nop 0
	global_load_lds_dwordx4 v132, s[42:43]
	s_add_i32 m0, s38, 0x2000
	s_nop 0
	global_load_lds_dwordx4 v136, s[42:43]
	s_mov_b32 m0, s53
	s_nop 0
	global_load_lds_dwordx4 v130, s[100:101]
	s_mov_b32 m0, s58
	s_nop 0
	global_load_lds_dwordx4 v134, s[100:101]
	s_waitcnt vmcnt(8)
	s_waitcnt lgkmcnt(0)
	s_barrier
	v_mfma_f32_16x16x32_f16 v[62:65], v[148:151], v[202:205], v[62:65]
	v_mfma_f32_16x16x32_f16 v[58:61], v[172:175], v[202:205], v[58:61]
	v_mfma_f32_16x16x32_f16 v[46:49], v[148:151], v[210:213], v[46:49]
	v_mfma_f32_16x16x32_f16 v[42:45], v[172:175], v[210:213], v[42:45]
	v_mfma_f32_16x16x32_f16 v[30:33], v[148:151], v[218:221], v[30:33]
	v_mfma_f32_16x16x32_f16 v[26:29], v[172:175], v[218:221], v[26:29]
	v_mfma_f32_16x16x32_f16 v[14:17], v[148:151], v[226:229], v[14:17]
	v_mfma_f32_16x16x32_f16 v[10:13], v[172:175], v[226:229], v[10:13]
	v_mfma_f32_16x16x32_f16 v[62:65], v[152:155], v[206:209], v[62:65]
	v_mfma_f32_16x16x32_f16 v[58:61], v[176:179], v[206:209], v[58:61]
	v_mfma_f32_16x16x32_f16 v[46:49], v[152:155], v[214:217], v[46:49]
	v_mfma_f32_16x16x32_f16 v[42:45], v[176:179], v[214:217], v[42:45]
	v_mfma_f32_16x16x32_f16 v[30:33], v[152:155], v[222:225], v[30:33]
	v_mfma_f32_16x16x32_f16 v[26:29], v[176:179], v[222:225], v[26:29]
	v_mfma_f32_16x16x32_f16 v[14:17], v[152:155], v[230:233], v[14:17]
	v_mfma_f32_16x16x32_f16 v[10:13], v[176:179], v[230:233], v[10:13]
	v_mfma_f32_16x16x32_f16 v[54:57], v[186:189], v[202:205], v[54:57]
	v_mfma_f32_16x16x32_f16 v[50:53], v[194:197], v[202:205], v[50:53]
	v_mfma_f32_16x16x32_f16 v[38:41], v[186:189], v[210:213], v[38:41]
	v_mfma_f32_16x16x32_f16 v[34:37], v[194:197], v[210:213], v[34:37]
	v_mfma_f32_16x16x32_f16 v[22:25], v[186:189], v[218:221], v[22:25]
	v_mfma_f32_16x16x32_f16 v[18:21], v[194:197], v[218:221], v[18:21]
	v_mfma_f32_16x16x32_f16 v[6:9], v[186:189], v[226:229], v[6:9]
	v_mfma_f32_16x16x32_f16 v[2:5], v[194:197], v[226:229], v[2:5]
	v_mfma_f32_16x16x32_f16 v[54:57], v[190:193], v[206:209], v[54:57]
	v_mfma_f32_16x16x32_f16 v[50:53], v[198:201], v[206:209], v[50:53]
	v_mfma_f32_16x16x32_f16 v[38:41], v[190:193], v[214:217], v[38:41]
	v_mfma_f32_16x16x32_f16 v[34:37], v[198:201], v[214:217], v[34:37]
	v_mfma_f32_16x16x32_f16 v[22:25], v[190:193], v[222:225], v[22:25]
	v_mfma_f32_16x16x32_f16 v[18:21], v[198:201], v[222:225], v[18:21]
	v_mfma_f32_16x16x32_f16 v[6:9], v[190:193], v[230:233], v[6:9]
	v_mfma_f32_16x16x32_f16 v[2:5], v[198:201], v[230:233], v[2:5]
	s_barrier
	s_add_i32 s67, s67, 2
	s_add_u32 s34, s34, 0x100
	s_addc_u32 s35, s35, 0
	s_add_u32 s63, s63, 0x100
	s_addc_u32 s66, s66, 0
	s_cmp_gt_u32 s67, 61
	s_cbranch_scc0 .LBB0_418
	s_setprio 0
	s_and_b64 vcc, exec, s[12:13]
	s_cbranch_vccz .LBB0_421
	s_barrier

.Lprio_P2b:
.LBB0_547:
	ds_read_b128 v[26:29], v191
	ds_read_b128 v[30:33], v191 offset:1024
	ds_read_b128 v[42:45], v191 offset:2048
	ds_read_b128 v[46:49], v191 offset:3072
	ds_read_b128 v[168:171], v192
	ds_read_b128 v[172:175], v192 offset:1024
	ds_read_b128 v[176:179], v192 offset:2048
	ds_read_b128 v[194:197], v192 offset:3072
	s_add_u32 s38, s34, 0xfff80080
	s_addc_u32 s39, s35, -1
	s_cmp_eq_u32 s74, 28
	s_cselect_b32 s45, s5, s39
	s_cselect_b32 s44, s7, s38
	s_cselect_b32 s43, s8, s73
	s_cselect_b32 s42, s65, s67
	s_add_i32 m0, s50, 0xc000
	ds_read_b128 v[198:201], v193
	ds_read_b128 v[202:205], v193 offset:1024
	ds_read_b128 v[206:209], v193 offset:2048
	ds_read_b128 v[210:213], v193 offset:3072
	ds_read_b128 v[214:217], v193 offset:4096
	ds_read_b128 v[218:221], v193 offset:5120
	ds_read_b128 v[222:225], v193 offset:6144
	ds_read_b128 v[226:229], v193 offset:7168
	global_load_lds_dwordx4 v156, s[34:35]
	s_add_i32 m0, s50, 0xe000
	s_nop 0
	global_load_lds_dwordx4 v158, s[34:35]
	s_waitcnt vmcnt(8)
	s_waitcnt lgkmcnt(0)
	s_barrier
	v_mfma_i32_16x16x64_i8 v[142:145], v[26:29], v[198:201], v[142:145]
	v_mfma_i32_16x16x64_i8 v[138:141], v[42:45], v[198:201], v[138:141]
	v_mfma_i32_16x16x64_i8 v[126:129], v[26:29], v[206:209], v[126:129]
	v_mfma_i32_16x16x64_i8 v[122:125], v[42:45], v[206:209], v[122:125]
	v_mfma_i32_16x16x64_i8 v[110:113], v[26:29], v[214:217], v[110:113]
	v_mfma_i32_16x16x64_i8 v[106:109], v[42:45], v[214:217], v[106:109]
	v_mfma_i32_16x16x64_i8 v[94:97], v[26:29], v[222:225], v[94:97]
	v_mfma_i32_16x16x64_i8 v[90:93], v[42:45], v[222:225], v[90:93]
	v_mfma_i32_16x16x64_i8 v[142:145], v[30:33], v[202:205], v[142:145]
	v_mfma_i32_16x16x64_i8 v[138:141], v[46:49], v[202:205], v[138:141]
	v_mfma_i32_16x16x64_i8 v[126:129], v[30:33], v[210:213], v[126:129]
	v_mfma_i32_16x16x64_i8 v[122:125], v[46:49], v[210:213], v[122:125]
	v_mfma_i32_16x16x64_i8 v[110:113], v[30:33], v[218:221], v[110:113]
	v_mfma_i32_16x16x64_i8 v[106:109], v[46:49], v[218:221], v[106:109]
	v_mfma_i32_16x16x64_i8 v[94:97], v[30:33], v[226:229], v[94:97]
	v_mfma_i32_16x16x64_i8 v[90:93], v[46:49], v[226:229], v[90:93]
	v_mfma_i32_16x16x64_i8 v[134:137], v[168:171], v[198:201], v[134:137]
	v_mfma_i32_16x16x64_i8 v[130:133], v[176:179], v[198:201], v[130:133]
	v_mfma_i32_16x16x64_i8 v[118:121], v[168:171], v[206:209], v[118:121]
	v_mfma_i32_16x16x64_i8 v[114:117], v[176:179], v[206:209], v[114:117]
	v_mfma_i32_16x16x64_i8 v[102:105], v[168:171], v[214:217], v[102:105]
	v_mfma_i32_16x16x64_i8 v[98:101], v[176:179], v[214:217], v[98:101]
	v_mfma_i32_16x16x64_i8 v[86:89], v[168:171], v[222:225], v[86:89]
	v_mfma_i32_16x16x64_i8 v[82:85], v[176:179], v[222:225], v[82:85]
	v_mfma_i32_16x16x64_i8 v[134:137], v[172:175], v[202:205], v[134:137]
	v_mfma_i32_16x16x64_i8 v[130:133], v[194:197], v[202:205], v[130:133]
	v_mfma_i32_16x16x64_i8 v[118:121], v[172:175], v[210:213], v[118:121]
	v_mfma_i32_16x16x64_i8 v[114:117], v[194:197], v[210:213], v[114:117]
	v_mfma_i32_16x16x64_i8 v[102:105], v[172:175], v[218:221], v[102:105]
	v_mfma_i32_16x16x64_i8 v[98:101], v[194:197], v[218:221], v[98:101]
	v_mfma_i32_16x16x64_i8 v[86:89], v[172:175], v[226:229], v[86:89]
	v_mfma_i32_16x16x64_i8 v[82:85], v[194:197], v[226:229], v[82:85]
	s_barrier
	s_add_u32 s98, s42, s12
	s_addc_u32 s99, s43, s13
	s_add_u32 s100, s44, s12
	s_addc_u32 s101, s45, s13
	s_add_i32 s38, s62, s47
	s_mov_b32 m0, s38
	ds_read_b128 v[198:201], v193 offset:16384
	ds_read_b128 v[202:205], v193 offset:17408
	ds_read_b128 v[206:209], v193 offset:18432
	ds_read_b128 v[210:213], v193 offset:19456
	ds_read_b128 v[214:217], v193 offset:20480
	ds_read_b128 v[218:221], v193 offset:21504
	ds_read_b128 v[222:225], v193 offset:22528
	ds_read_b128 v[226:229], v193 offset:23552
	global_load_lds_dwordx4 v148, s[42:43]
	s_add_i32 m0, s38, 0x2000
	s_add_u32 s76, s42, 0x80000
	s_addc_u32 s77, s43, 0
	s_add_i32 s38, s63, s47
	global_load_lds_dwordx4 v152, s[42:43]
	s_mov_b32 m0, s38
	s_nop 0
	global_load_lds_dwordx4 v148, s[76:77]
	s_add_i32 m0, s38, 0x2000
	s_nop 0
	global_load_lds_dwordx4 v152, s[76:77]
	s_mov_b32 m0, s50
	s_nop 0
	global_load_lds_dwordx4 v146, s[44:45]
	s_mov_b32 m0, s51
	s_nop 0
	global_load_lds_dwordx4 v150, s[44:45]
	s_waitcnt vmcnt(8)
	s_waitcnt lgkmcnt(0)
	s_barrier
	v_mfma_i32_16x16x64_i8 v[78:81], v[26:29], v[198:201], v[78:81]
	v_mfma_i32_16x16x64_i8 v[74:77], v[42:45], v[198:201], v[74:77]
	v_mfma_i32_16x16x64_i8 v[62:65], v[26:29], v[206:209], v[62:65]
	v_mfma_i32_16x16x64_i8 v[58:61], v[42:45], v[206:209], v[58:61]
	v_mfma_i32_16x16x64_i8 v[38:41], v[26:29], v[214:217], v[38:41]
	v_mfma_i32_16x16x64_i8 v[34:37], v[42:45], v[214:217], v[34:37]
	v_mfma_i32_16x16x64_i8 v[14:17], v[26:29], v[222:225], v[14:17]
	v_mfma_i32_16x16x64_i8 v[10:13], v[42:45], v[222:225], v[10:13]
	v_mfma_i32_16x16x64_i8 v[78:81], v[30:33], v[202:205], v[78:81]
	v_mfma_i32_16x16x64_i8 v[74:77], v[46:49], v[202:205], v[74:77]
	v_mfma_i32_16x16x64_i8 v[62:65], v[30:33], v[210:213], v[62:65]
	v_mfma_i32_16x16x64_i8 v[58:61], v[46:49], v[210:213], v[58:61]
	v_mfma_i32_16x16x64_i8 v[38:41], v[30:33], v[218:221], v[38:41]
	v_mfma_i32_16x16x64_i8 v[34:37], v[46:49], v[218:221], v[34:37]
	v_mfma_i32_16x16x64_i8 v[14:17], v[30:33], v[226:229], v[14:17]
	v_mfma_i32_16x16x64_i8 v[10:13], v[46:49], v[226:229], v[10:13]
	v_mfma_i32_16x16x64_i8 v[22:25], v[168:171], v[214:217], v[22:25]
	v_mfma_i32_16x16x64_i8 v[18:21], v[176:179], v[214:217], v[18:21]
	v_mfma_i32_16x16x64_i8 v[6:9], v[168:171], v[222:225], v[6:9]
	v_mfma_i32_16x16x64_i8 v[2:5], v[176:179], v[222:225], v[2:5]
	v_mfma_i32_16x16x64_i8 v[26:29], v[168:171], v[198:201], v[70:73]
	v_mfma_i32_16x16x64_i8 v[30:33], v[176:179], v[198:201], v[66:69]
	v_mfma_i32_16x16x64_i8 v[42:45], v[168:171], v[206:209], v[54:57]
	v_mfma_i32_16x16x64_i8 v[46:49], v[176:179], v[206:209], v[50:53]
	v_mfma_i32_16x16x64_i8 v[22:25], v[172:175], v[218:221], v[22:25]
	v_mfma_i32_16x16x64_i8 v[18:21], v[194:197], v[218:221], v[18:21]
	v_mfma_i32_16x16x64_i8 v[6:9], v[172:175], v[226:229], v[6:9]
	v_mfma_i32_16x16x64_i8 v[2:5], v[194:197], v[226:229], v[2:5]
	v_mfma_i32_16x16x64_i8 v[26:29], v[172:175], v[202:205], v[26:29]
	v_mfma_i32_16x16x64_i8 v[30:33], v[194:197], v[202:205], v[30:33]
	v_mfma_i32_16x16x64_i8 v[42:45], v[172:175], v[210:213], v[42:45]
	v_mfma_i32_16x16x64_i8 v[46:49], v[194:197], v[210:213], v[46:49]
	s_barrier
	s_add_i32 s38, 0, 0x18000
	s_add_i32 s39, 0, 0x1c000
	v_add_u32_e32 v70, s38, v188
	v_add_u32_e32 v154, s39, v188
	ds_read_b128 v[50:53], v70
	ds_read_b128 v[54:57], v70 offset:1024
	ds_read_b128 v[66:69], v70 offset:2048
	ds_read_b128 v[70:73], v70 offset:3072
	ds_read_b128 v[168:171], v154
	ds_read_b128 v[172:175], v154 offset:1024
	ds_read_b128 v[176:179], v154 offset:2048
	ds_read_b128 v[194:197], v154 offset:3072
	s_add_u32 s44, s44, 0x80000
	s_addc_u32 s45, s45, 0
	s_mov_b32 m0, s52
	ds_read_b128 v[198:201], v193 offset:32768
	ds_read_b128 v[202:205], v193 offset:33792
	ds_read_b128 v[206:209], v193 offset:34816
	ds_read_b128 v[210:213], v193 offset:35840
	ds_read_b128 v[214:217], v193 offset:36864
	ds_read_b128 v[218:221], v193 offset:37888
	ds_read_b128 v[222:225], v193 offset:38912
	ds_read_b128 v[226:229], v193 offset:39936
	global_load_lds_dwordx4 v146, s[44:45]
	s_mov_b32 m0, s53
	s_nop 0
	global_load_lds_dwordx4 v150, s[44:45]
	s_waitcnt vmcnt(8)
	s_waitcnt lgkmcnt(0)
	s_barrier
	v_mfma_i32_16x16x64_i8 v[142:145], v[50:53], v[198:201], v[142:145]
	v_mfma_i32_16x16x64_i8 v[138:141], v[66:69], v[198:201], v[138:141]
	v_mfma_i32_16x16x64_i8 v[126:129], v[50:53], v[206:209], v[126:129]
	v_mfma_i32_16x16x64_i8 v[122:125], v[66:69], v[206:209], v[122:125]
	v_mfma_i32_16x16x64_i8 v[110:113], v[50:53], v[214:217], v[110:113]
	v_mfma_i32_16x16x64_i8 v[106:109], v[66:69], v[214:217], v[106:109]
	v_mfma_i32_16x16x64_i8 v[94:97], v[50:53], v[222:225], v[94:97]
	v_mfma_i32_16x16x64_i8 v[90:93], v[66:69], v[222:225], v[90:93]
	v_mfma_i32_16x16x64_i8 v[142:145], v[54:57], v[202:205], v[142:145]
	v_mfma_i32_16x16x64_i8 v[138:141], v[70:73], v[202:205], v[138:141]
	v_mfma_i32_16x16x64_i8 v[126:129], v[54:57], v[210:213], v[126:129]
	v_mfma_i32_16x16x64_i8 v[122:125], v[70:73], v[210:213], v[122:125]
	v_mfma_i32_16x16x64_i8 v[110:113], v[54:57], v[218:221], v[110:113]
	v_mfma_i32_16x16x64_i8 v[106:109], v[70:73], v[218:221], v[106:109]
	v_mfma_i32_16x16x64_i8 v[94:97], v[54:57], v[226:229], v[94:97]
	v_mfma_i32_16x16x64_i8 v[90:93], v[70:73], v[226:229], v[90:93]
	v_mfma_i32_16x16x64_i8 v[134:137], v[168:171], v[198:201], v[134:137]
	v_mfma_i32_16x16x64_i8 v[130:133], v[176:179], v[198:201], v[130:133]
	v_mfma_i32_16x16x64_i8 v[118:121], v[168:171], v[206:209], v[118:121]
	v_mfma_i32_16x16x64_i8 v[114:117], v[176:179], v[206:209], v[114:117]
	v_mfma_i32_16x16x64_i8 v[102:105], v[168:171], v[214:217], v[102:105]
	v_mfma_i32_16x16x64_i8 v[98:101], v[176:179], v[214:217], v[98:101]
	v_mfma_i32_16x16x64_i8 v[86:89], v[168:171], v[222:225], v[86:89]
	v_mfma_i32_16x16x64_i8 v[82:85], v[176:179], v[222:225], v[82:85]
	v_mfma_i32_16x16x64_i8 v[134:137], v[172:175], v[202:205], v[134:137]
	v_mfma_i32_16x16x64_i8 v[130:133], v[194:197], v[202:205], v[130:133]
	v_mfma_i32_16x16x64_i8 v[118:121], v[172:175], v[210:213], v[118:121]
	v_mfma_i32_16x16x64_i8 v[114:117], v[194:197], v[210:213], v[114:117]
	v_mfma_i32_16x16x64_i8 v[102:105], v[172:175], v[218:221], v[102:105]
	v_mfma_i32_16x16x64_i8 v[98:101], v[194:197], v[218:221], v[98:101]
	v_mfma_i32_16x16x64_i8 v[86:89], v[172:175], v[226:229], v[86:89]
	v_mfma_i32_16x16x64_i8 v[82:85], v[194:197], v[226:229], v[82:85]
	s_barrier
	s_add_i32 s38, s38, s47
	s_mov_b32 m0, s38
	ds_read_b128 v[198:201], v193 offset:49152
	ds_read_b128 v[202:205], v193 offset:50176
	ds_read_b128 v[206:209], v193 offset:51200
	ds_read_b128 v[210:213], v193 offset:52224
	ds_read_b128 v[214:217], v193 offset:53248
	ds_read_b128 v[218:221], v193 offset:54272
	ds_read_b128 v[222:225], v193 offset:55296
	ds_read_b128 v[226:229], v193 offset:56320
	global_load_lds_dwordx4 v148, s[98:99]
	s_add_i32 m0, s38, 0x2000
	s_add_u32 s42, s42, 0x80080
	s_addc_u32 s43, s43, 0
	s_add_i32 s38, s39, s47
	global_load_lds_dwordx4 v152, s[98:99]
	s_mov_b32 m0, s38
	s_nop 0
	global_load_lds_dwordx4 v148, s[42:43]
	s_add_i32 m0, s38, 0x2000
	s_nop 0
	global_load_lds_dwordx4 v152, s[42:43]
	s_mov_b32 m0, s58
	s_nop 0
	global_load_lds_dwordx4 v146, s[100:101]
	s_mov_b32 m0, s59
	s_nop 0
	global_load_lds_dwordx4 v150, s[100:101]
	s_waitcnt vmcnt(8)
	s_waitcnt lgkmcnt(0)
	s_barrier
	v_mfma_i32_16x16x64_i8 v[78:81], v[50:53], v[198:201], v[78:81]
	v_mfma_i32_16x16x64_i8 v[74:77], v[66:69], v[198:201], v[74:77]
	v_mfma_i32_16x16x64_i8 v[62:65], v[50:53], v[206:209], v[62:65]
	v_mfma_i32_16x16x64_i8 v[58:61], v[66:69], v[206:209], v[58:61]
	v_mfma_i32_16x16x64_i8 v[38:41], v[50:53], v[214:217], v[38:41]
	v_mfma_i32_16x16x64_i8 v[34:37], v[66:69], v[214:217], v[34:37]
	v_mfma_i32_16x16x64_i8 v[14:17], v[50:53], v[222:225], v[14:17]
	v_mfma_i32_16x16x64_i8 v[10:13], v[66:69], v[222:225], v[10:13]
	v_mfma_i32_16x16x64_i8 v[78:81], v[54:57], v[202:205], v[78:81]
	v_mfma_i32_16x16x64_i8 v[74:77], v[70:73], v[202:205], v[74:77]
	v_mfma_i32_16x16x64_i8 v[62:65], v[54:57], v[210:213], v[62:65]
	v_mfma_i32_16x16x64_i8 v[58:61], v[70:73], v[210:213], v[58:61]
	v_mfma_i32_16x16x64_i8 v[38:41], v[54:57], v[218:221], v[38:41]
	v_mfma_i32_16x16x64_i8 v[34:37], v[70:73], v[218:221], v[34:37]
	v_mfma_i32_16x16x64_i8 v[14:17], v[54:57], v[226:229], v[14:17]
	v_mfma_i32_16x16x64_i8 v[10:13], v[70:73], v[226:229], v[10:13]
	v_mfma_i32_16x16x64_i8 v[26:29], v[168:171], v[198:201], v[26:29]
	v_mfma_i32_16x16x64_i8 v[70:73], v[172:175], v[202:205], v[26:29]
	v_mfma_i32_16x16x64_i8 v[26:29], v[176:179], v[198:201], v[30:33]
	v_mfma_i32_16x16x64_i8 v[66:69], v[194:197], v[202:205], v[26:29]
	v_mfma_i32_16x16x64_i8 v[26:29], v[168:171], v[206:209], v[42:45]
	v_mfma_i32_16x16x64_i8 v[54:57], v[172:175], v[210:213], v[26:29]
	v_mfma_i32_16x16x64_i8 v[26:29], v[176:179], v[206:209], v[46:49]
	v_mfma_i32_16x16x64_i8 v[22:25], v[168:171], v[214:217], v[22:25]
	v_mfma_i32_16x16x64_i8 v[18:21], v[176:179], v[214:217], v[18:21]
	v_mfma_i32_16x16x64_i8 v[6:9], v[168:171], v[222:225], v[6:9]
	v_mfma_i32_16x16x64_i8 v[2:5], v[176:179], v[222:225], v[2:5]
	v_mfma_i32_16x16x64_i8 v[50:53], v[194:197], v[210:213], v[26:29]
	v_mfma_i32_16x16x64_i8 v[22:25], v[172:175], v[218:221], v[22:25]
	v_mfma_i32_16x16x64_i8 v[18:21], v[194:197], v[218:221], v[18:21]
	v_mfma_i32_16x16x64_i8 v[6:9], v[172:175], v[226:229], v[6:9]
	v_mfma_i32_16x16x64_i8 v[2:5], v[194:197], v[226:229], v[2:5]
	s_barrier
	s_add_i32 s74, s74, 2
	s_add_u32 s34, s34, 0x100
	s_addc_u32 s35, s35, 0
	s_add_u32 s67, s67, 0x100
	s_addc_u32 s73, s73, 0
	s_cmp_gt_u32 s74, 29
	s_cbranch_scc0 .LBB0_547
	s_setprio 0
	s_and_b64 vcc, exec, s[14:15]
	s_cbranch_vccz .LBB0_550
	s_barrier

.Lprio_P2c:
.LBB0_673:
	ds_read_b128 v[122:125], v167
	ds_read_b128 v[126:129], v167 offset:1024
	ds_read_b128 v[130:133], v167 offset:2048
	ds_read_b128 v[134:137], v167 offset:3072
	ds_read_b128 v[174:177], v171
	ds_read_b128 v[178:181], v171 offset:1024
	ds_read_b128 v[182:185], v171 offset:2048
	ds_read_b128 v[186:189], v171 offset:3072
	s_add_u32 s38, s44, 0xfff80080
	s_addc_u32 s39, s45, -1
	s_cmp_eq_u32 s77, 28
	s_cselect_b32 s47, s25, s39
	s_cselect_b32 s46, s73, s38
	s_cselect_b32 s43, s15, s76
	s_cselect_b32 s42, s74, s75
	s_add_i32 m0, s35, 0xc000
	ds_read_b128 v[190:193], v172
	ds_read_b128 v[194:197], v172 offset:1024
	ds_read_b128 v[198:201], v172 offset:2048
	ds_read_b128 v[202:205], v172 offset:3072
	ds_read_b128 v[206:209], v172 offset:4096
	ds_read_b128 v[210:213], v172 offset:5120
	ds_read_b128 v[214:217], v172 offset:6144
	ds_read_b128 v[218:221], v172 offset:7168
	global_load_lds_dwordx4 v156, s[44:45]
	s_add_i32 m0, s35, 0xe000
	s_nop 0
	global_load_lds_dwordx4 v158, s[44:45]
	s_waitcnt vmcnt(8)
	s_waitcnt lgkmcnt(0)
	s_barrier
	v_mfma_i32_16x16x64_i8 v[142:145], v[122:125], v[190:193], v[142:145]
	v_mfma_i32_16x16x64_i8 v[138:141], v[130:133], v[190:193], v[138:141]
	v_mfma_i32_16x16x64_i8 v[110:113], v[122:125], v[198:201], v[110:113]
	v_mfma_i32_16x16x64_i8 v[106:109], v[130:133], v[198:201], v[106:109]
	v_mfma_i32_16x16x64_i8 v[94:97], v[122:125], v[206:209], v[94:97]
	v_mfma_i32_16x16x64_i8 v[90:93], v[130:133], v[206:209], v[90:93]
	v_mfma_i32_16x16x64_i8 v[78:81], v[122:125], v[214:217], v[78:81]
	v_mfma_i32_16x16x64_i8 v[74:77], v[130:133], v[214:217], v[74:77]
	v_mfma_i32_16x16x64_i8 v[142:145], v[126:129], v[194:197], v[142:145]
	v_mfma_i32_16x16x64_i8 v[138:141], v[134:137], v[194:197], v[138:141]
	v_mfma_i32_16x16x64_i8 v[110:113], v[126:129], v[202:205], v[110:113]
	v_mfma_i32_16x16x64_i8 v[106:109], v[134:137], v[202:205], v[106:109]
	v_mfma_i32_16x16x64_i8 v[94:97], v[126:129], v[210:213], v[94:97]
	v_mfma_i32_16x16x64_i8 v[90:93], v[134:137], v[210:213], v[90:93]
	v_mfma_i32_16x16x64_i8 v[78:81], v[126:129], v[218:221], v[78:81]
	v_mfma_i32_16x16x64_i8 v[74:77], v[134:137], v[218:221], v[74:77]
	v_mfma_i32_16x16x64_i8 v[118:121], v[174:177], v[190:193], v[118:121]
	v_mfma_i32_16x16x64_i8 v[114:117], v[182:185], v[190:193], v[114:117]
	v_mfma_i32_16x16x64_i8 v[102:105], v[174:177], v[198:201], v[102:105]
	v_mfma_i32_16x16x64_i8 v[98:101], v[182:185], v[198:201], v[98:101]
	v_mfma_i32_16x16x64_i8 v[86:89], v[174:177], v[206:209], v[86:89]
	v_mfma_i32_16x16x64_i8 v[82:85], v[182:185], v[206:209], v[82:85]
	v_mfma_i32_16x16x64_i8 v[70:73], v[174:177], v[214:217], v[70:73]
	v_mfma_i32_16x16x64_i8 v[66:69], v[182:185], v[214:217], v[66:69]
	v_mfma_i32_16x16x64_i8 v[118:121], v[178:181], v[194:197], v[118:121]
	v_mfma_i32_16x16x64_i8 v[114:117], v[186:189], v[194:197], v[114:117]
	v_mfma_i32_16x16x64_i8 v[102:105], v[178:181], v[202:205], v[102:105]
	v_mfma_i32_16x16x64_i8 v[98:101], v[186:189], v[202:205], v[98:101]
	v_mfma_i32_16x16x64_i8 v[86:89], v[178:181], v[210:213], v[86:89]
	v_mfma_i32_16x16x64_i8 v[82:85], v[186:189], v[210:213], v[82:85]
	v_mfma_i32_16x16x64_i8 v[70:73], v[178:181], v[218:221], v[70:73]
	v_mfma_i32_16x16x64_i8 v[66:69], v[186:189], v[218:221], v[66:69]
	s_barrier
	s_add_u32 s98, s42, s6
	s_addc_u32 s99, s43, s7
	s_add_u32 s100, s46, s6
	s_addc_u32 s101, s47, s7
	s_add_i32 s38, s66, s52
	s_mov_b32 m0, s38
	ds_read_b128 v[190:193], v172 offset:16384
	ds_read_b128 v[194:197], v172 offset:17408
	ds_read_b128 v[198:201], v172 offset:18432
	ds_read_b128 v[202:205], v172 offset:19456
	ds_read_b128 v[206:209], v172 offset:20480
	ds_read_b128 v[210:213], v172 offset:21504
	ds_read_b128 v[214:217], v172 offset:22528
	ds_read_b128 v[218:221], v172 offset:23552
	global_load_lds_dwordx4 v148, s[42:43]
	s_add_i32 m0, s38, 0x2000
	s_add_u32 s78, s42, 0x80000
	s_addc_u32 s79, s43, 0
	s_add_i32 s38, s67, s52
	global_load_lds_dwordx4 v152, s[42:43]
	s_mov_b32 m0, s38
	s_nop 0
	global_load_lds_dwordx4 v148, s[78:79]
	s_add_i32 m0, s38, 0x2000
	s_nop 0
	global_load_lds_dwordx4 v152, s[78:79]
	s_mov_b32 m0, s35
	s_nop 0
	global_load_lds_dwordx4 v146, s[46:47]
	s_mov_b32 m0, s53
	s_nop 0
	global_load_lds_dwordx4 v150, s[46:47]
	s_waitcnt vmcnt(8)
	s_waitcnt lgkmcnt(0)
	s_barrier
	v_mfma_i32_16x16x64_i8 v[62:65], v[122:125], v[190:193], v[62:65]
	v_mfma_i32_16x16x64_i8 v[58:61], v[130:133], v[190:193], v[58:61]
	v_mfma_i32_16x16x64_i8 v[46:49], v[122:125], v[198:201], v[46:49]
	v_mfma_i32_16x16x64_i8 v[42:45], v[130:133], v[198:201], v[42:45]
	v_mfma_i32_16x16x64_i8 v[30:33], v[122:125], v[206:209], v[30:33]
	v_mfma_i32_16x16x64_i8 v[26:29], v[130:133], v[206:209], v[26:29]
	v_mfma_i32_16x16x64_i8 v[14:17], v[122:125], v[214:217], v[14:17]
	v_mfma_i32_16x16x64_i8 v[10:13], v[130:133], v[214:217], v[10:13]
	v_mfma_i32_16x16x64_i8 v[62:65], v[126:129], v[194:197], v[62:65]
	v_mfma_i32_16x16x64_i8 v[58:61], v[134:137], v[194:197], v[58:61]
	v_mfma_i32_16x16x64_i8 v[46:49], v[126:129], v[202:205], v[46:49]
	v_mfma_i32_16x16x64_i8 v[42:45], v[134:137], v[202:205], v[42:45]
	v_mfma_i32_16x16x64_i8 v[30:33], v[126:129], v[210:213], v[30:33]
	v_mfma_i32_16x16x64_i8 v[26:29], v[134:137], v[210:213], v[26:29]
	v_mfma_i32_16x16x64_i8 v[14:17], v[126:129], v[218:221], v[14:17]
	v_mfma_i32_16x16x64_i8 v[10:13], v[134:137], v[218:221], v[10:13]
	v_mfma_i32_16x16x64_i8 v[54:57], v[174:177], v[190:193], v[54:57]
	v_mfma_i32_16x16x64_i8 v[50:53], v[182:185], v[190:193], v[50:53]
	v_mfma_i32_16x16x64_i8 v[38:41], v[174:177], v[198:201], v[38:41]
	v_mfma_i32_16x16x64_i8 v[34:37], v[182:185], v[198:201], v[34:37]
	v_mfma_i32_16x16x64_i8 v[22:25], v[174:177], v[206:209], v[22:25]
	v_mfma_i32_16x16x64_i8 v[18:21], v[182:185], v[206:209], v[18:21]
	v_mfma_i32_16x16x64_i8 v[6:9], v[174:177], v[214:217], v[6:9]
	v_mfma_i32_16x16x64_i8 v[2:5], v[182:185], v[214:217], v[2:5]
	v_mfma_i32_16x16x64_i8 v[54:57], v[178:181], v[194:197], v[54:57]
	v_mfma_i32_16x16x64_i8 v[50:53], v[186:189], v[194:197], v[50:53]
	v_mfma_i32_16x16x64_i8 v[38:41], v[178:181], v[202:205], v[38:41]
	v_mfma_i32_16x16x64_i8 v[34:37], v[186:189], v[202:205], v[34:37]
	v_mfma_i32_16x16x64_i8 v[22:25], v[178:181], v[210:213], v[22:25]
	v_mfma_i32_16x16x64_i8 v[18:21], v[186:189], v[210:213], v[18:21]
	v_mfma_i32_16x16x64_i8 v[6:9], v[178:181], v[218:221], v[6:9]
	v_mfma_i32_16x16x64_i8 v[2:5], v[186:189], v[218:221], v[2:5]
	s_barrier
	s_add_i32 s38, 0, 0x18000
	s_add_i32 s39, 0, 0x1c000
	v_add_u32_e32 v134, s38, v169
	v_add_u32_e32 v154, s39, v169
	ds_read_b128 v[122:125], v134
	ds_read_b128 v[126:129], v134 offset:1024
	ds_read_b128 v[130:133], v134 offset:2048
	ds_read_b128 v[134:137], v134 offset:3072
	ds_read_b128 v[174:177], v154
	ds_read_b128 v[178:181], v154 offset:1024
	ds_read_b128 v[182:185], v154 offset:2048
	ds_read_b128 v[186:189], v154 offset:3072
	s_add_u32 s46, s46, 0x80000
	s_addc_u32 s47, s47, 0
	s_mov_b32 m0, s58
	ds_read_b128 v[190:193], v172 offset:32768
	ds_read_b128 v[194:197], v172 offset:33792
	ds_read_b128 v[198:201], v172 offset:34816
	ds_read_b128 v[202:205], v172 offset:35840
	ds_read_b128 v[206:209], v172 offset:36864
	ds_read_b128 v[210:213], v172 offset:37888
	ds_read_b128 v[214:217], v172 offset:38912
	ds_read_b128 v[218:221], v172 offset:39936
	global_load_lds_dwordx4 v146, s[46:47]
	s_mov_b32 m0, s59
	s_nop 0
	global_load_lds_dwordx4 v150, s[46:47]
	s_waitcnt vmcnt(8)
	s_waitcnt lgkmcnt(0)
	s_barrier
	v_mfma_i32_16x16x64_i8 v[142:145], v[122:125], v[190:193], v[142:145]
	v_mfma_i32_16x16x64_i8 v[138:141], v[130:133], v[190:193], v[138:141]
	v_mfma_i32_16x16x64_i8 v[110:113], v[122:125], v[198:201], v[110:113]
	v_mfma_i32_16x16x64_i8 v[106:109], v[130:133], v[198:201], v[106:109]
	v_mfma_i32_16x16x64_i8 v[94:97], v[122:125], v[206:209], v[94:97]
	v_mfma_i32_16x16x64_i8 v[90:93], v[130:133], v[206:209], v[90:93]
	v_mfma_i32_16x16x64_i8 v[78:81], v[122:125], v[214:217], v[78:81]
	v_mfma_i32_16x16x64_i8 v[74:77], v[130:133], v[214:217], v[74:77]
	v_mfma_i32_16x16x64_i8 v[142:145], v[126:129], v[194:197], v[142:145]
	v_mfma_i32_16x16x64_i8 v[138:141], v[134:137], v[194:197], v[138:141]
	v_mfma_i32_16x16x64_i8 v[110:113], v[126:129], v[202:205], v[110:113]
	v_mfma_i32_16x16x64_i8 v[106:109], v[134:137], v[202:205], v[106:109]
	v_mfma_i32_16x16x64_i8 v[94:97], v[126:129], v[210:213], v[94:97]
	v_mfma_i32_16x16x64_i8 v[90:93], v[134:137], v[210:213], v[90:93]
	v_mfma_i32_16x16x64_i8 v[78:81], v[126:129], v[218:221], v[78:81]
	v_mfma_i32_16x16x64_i8 v[74:77], v[134:137], v[218:221], v[74:77]
	v_mfma_i32_16x16x64_i8 v[118:121], v[174:177], v[190:193], v[118:121]
	v_mfma_i32_16x16x64_i8 v[114:117], v[182:185], v[190:193], v[114:117]
	v_mfma_i32_16x16x64_i8 v[102:105], v[174:177], v[198:201], v[102:105]
	v_mfma_i32_16x16x64_i8 v[98:101], v[182:185], v[198:201], v[98:101]
	v_mfma_i32_16x16x64_i8 v[86:89], v[174:177], v[206:209], v[86:89]
	v_mfma_i32_16x16x64_i8 v[82:85], v[182:185], v[206:209], v[82:85]
	v_mfma_i32_16x16x64_i8 v[70:73], v[174:177], v[214:217], v[70:73]
	v_mfma_i32_16x16x64_i8 v[66:69], v[182:185], v[214:217], v[66:69]
	v_mfma_i32_16x16x64_i8 v[118:121], v[178:181], v[194:197], v[118:121]
	v_mfma_i32_16x16x64_i8 v[114:117], v[186:189], v[194:197], v[114:117]
	v_mfma_i32_16x16x64_i8 v[102:105], v[178:181], v[202:205], v[102:105]
	v_mfma_i32_16x16x64_i8 v[98:101], v[186:189], v[202:205], v[98:101]
	v_mfma_i32_16x16x64_i8 v[86:89], v[178:181], v[210:213], v[86:89]
	v_mfma_i32_16x16x64_i8 v[82:85], v[186:189], v[210:213], v[82:85]
	v_mfma_i32_16x16x64_i8 v[70:73], v[178:181], v[218:221], v[70:73]
	v_mfma_i32_16x16x64_i8 v[66:69], v[186:189], v[218:221], v[66:69]
	s_barrier
	s_add_i32 s38, s38, s52
	s_mov_b32 m0, s38
	ds_read_b128 v[190:193], v172 offset:49152
	ds_read_b128 v[194:197], v172 offset:50176
	ds_read_b128 v[198:201], v172 offset:51200
	ds_read_b128 v[202:205], v172 offset:52224
	ds_read_b128 v[206:209], v172 offset:53248
	ds_read_b128 v[210:213], v172 offset:54272
	ds_read_b128 v[214:217], v172 offset:55296
	ds_read_b128 v[218:221], v172 offset:56320
	global_load_lds_dwordx4 v148, s[98:99]
	s_add_i32 m0, s38, 0x2000
	s_add_u32 s42, s42, 0x80080
	s_addc_u32 s43, s43, 0
	s_add_i32 s38, s39, s52
	global_load_lds_dwordx4 v152, s[98:99]
	s_mov_b32 m0, s38
	s_nop 0
	global_load_lds_dwordx4 v148, s[42:43]
	s_add_i32 m0, s38, 0x2000
	s_nop 0
	global_load_lds_dwordx4 v152, s[42:43]
	s_mov_b32 m0, s61
	s_nop 0
	global_load_lds_dwordx4 v146, s[100:101]
	s_mov_b32 m0, s62
	s_nop 0
	global_load_lds_dwordx4 v150, s[100:101]
	s_waitcnt vmcnt(8)
	s_waitcnt lgkmcnt(0)
	s_barrier
	v_mfma_i32_16x16x64_i8 v[62:65], v[122:125], v[190:193], v[62:65]
	v_mfma_i32_16x16x64_i8 v[58:61], v[130:133], v[190:193], v[58:61]
	v_mfma_i32_16x16x64_i8 v[46:49], v[122:125], v[198:201], v[46:49]
	v_mfma_i32_16x16x64_i8 v[42:45], v[130:133], v[198:201], v[42:45]
	v_mfma_i32_16x16x64_i8 v[30:33], v[122:125], v[206:209], v[30:33]
	v_mfma_i32_16x16x64_i8 v[26:29], v[130:133], v[206:209], v[26:29]
	v_mfma_i32_16x16x64_i8 v[14:17], v[122:125], v[214:217], v[14:17]
	v_mfma_i32_16x16x64_i8 v[10:13], v[130:133], v[214:217], v[10:13]
	v_mfma_i32_16x16x64_i8 v[62:65], v[126:129], v[194:197], v[62:65]
	v_mfma_i32_16x16x64_i8 v[58:61], v[134:137], v[194:197], v[58:61]
	v_mfma_i32_16x16x64_i8 v[46:49], v[126:129], v[202:205], v[46:49]
	v_mfma_i32_16x16x64_i8 v[42:45], v[134:137], v[202:205], v[42:45]
	v_mfma_i32_16x16x64_i8 v[30:33], v[126:129], v[210:213], v[30:33]
	v_mfma_i32_16x16x64_i8 v[26:29], v[134:137], v[210:213], v[26:29]
	v_mfma_i32_16x16x64_i8 v[14:17], v[126:129], v[218:221], v[14:17]
	v_mfma_i32_16x16x64_i8 v[10:13], v[134:137], v[218:221], v[10:13]
	v_mfma_i32_16x16x64_i8 v[54:57], v[174:177], v[190:193], v[54:57]
	v_mfma_i32_16x16x64_i8 v[50:53], v[182:185], v[190:193], v[50:53]
	v_mfma_i32_16x16x64_i8 v[38:41], v[174:177], v[198:201], v[38:41]
	v_mfma_i32_16x16x64_i8 v[34:37], v[182:185], v[198:201], v[34:37]
	v_mfma_i32_16x16x64_i8 v[22:25], v[174:177], v[206:209], v[22:25]
	v_mfma_i32_16x16x64_i8 v[18:21], v[182:185], v[206:209], v[18:21]
	v_mfma_i32_16x16x64_i8 v[6:9], v[174:177], v[214:217], v[6:9]
	v_mfma_i32_16x16x64_i8 v[2:5], v[182:185], v[214:217], v[2:5]
	v_mfma_i32_16x16x64_i8 v[54:57], v[178:181], v[194:197], v[54:57]
	v_mfma_i32_16x16x64_i8 v[50:53], v[186:189], v[194:197], v[50:53]
	v_mfma_i32_16x16x64_i8 v[38:41], v[178:181], v[202:205], v[38:41]
	v_mfma_i32_16x16x64_i8 v[34:37], v[186:189], v[202:205], v[34:37]
	v_mfma_i32_16x16x64_i8 v[22:25], v[178:181], v[210:213], v[22:25]
	v_mfma_i32_16x16x64_i8 v[18:21], v[186:189], v[210:213], v[18:21]
	v_mfma_i32_16x16x64_i8 v[6:9], v[178:181], v[218:221], v[6:9]
	v_mfma_i32_16x16x64_i8 v[2:5], v[186:189], v[218:221], v[2:5]
	s_barrier
	s_add_i32 s77, s77, 2
	s_add_u32 s44, s44, 0x100
	s_addc_u32 s45, s45, 0
	s_add_u32 s75, s75, 0x100
	s_addc_u32 s76, s76, 0
	s_cmp_gt_u32 s77, 29
	s_cbranch_scc0 .LBB0_673
	s_setprio 0
	s_and_b64 vcc, exec, s[8:9]
	s_cbranch_vccz .LBB0_676
	s_barrier

.Lprio_P6:
.LBB0_1489:
	ds_read_b128 v[122:125], v169
	ds_read_b128 v[126:129], v169 offset:1024
	ds_read_b128 v[130:133], v169 offset:2048
	ds_read_b128 v[134:137], v169 offset:3072
	ds_read_b128 v[172:175], v170
	ds_read_b128 v[176:179], v170 offset:1024
	ds_read_b128 v[180:183], v170 offset:2048
	ds_read_b128 v[184:187], v170 offset:3072
	s_add_u32 s26, s24, 0xfff80080
	s_addc_u32 s27, s25, -1
	s_cmp_eq_u32 s53, 28
	s_cselect_b32 s29, s17, s27
	s_cselect_b32 s28, s49, s26
	s_cselect_b32 s27, s15, s52
	s_cselect_b32 s26, s50, s51
	s_add_i32 m0, s23, 0xc000
	ds_read_b128 v[188:191], v171
	ds_read_b128 v[192:195], v171 offset:1024
	ds_read_b128 v[196:199], v171 offset:2048
	ds_read_b128 v[200:203], v171 offset:3072
	ds_read_b128 v[204:207], v171 offset:4096
	ds_read_b128 v[208:211], v171 offset:5120
	ds_read_b128 v[212:215], v171 offset:6144
	ds_read_b128 v[216:219], v171 offset:7168
	global_load_lds_dwordx4 v156, s[24:25]
	s_add_i32 m0, s23, 0xe000
	s_nop 0
	global_load_lds_dwordx4 v158, s[24:25]
	s_waitcnt vmcnt(8)
	s_waitcnt lgkmcnt(0)
	s_barrier
	v_mfma_i32_16x16x64_i8 v[142:145], v[122:125], v[188:191], v[142:145]
	v_mfma_i32_16x16x64_i8 v[138:141], v[130:133], v[188:191], v[138:141]
	v_mfma_i32_16x16x64_i8 v[110:113], v[122:125], v[196:199], v[110:113]
	v_mfma_i32_16x16x64_i8 v[106:109], v[130:133], v[196:199], v[106:109]
	v_mfma_i32_16x16x64_i8 v[94:97], v[122:125], v[204:207], v[94:97]
	v_mfma_i32_16x16x64_i8 v[90:93], v[130:133], v[204:207], v[90:93]
	v_mfma_i32_16x16x64_i8 v[78:81], v[122:125], v[212:215], v[78:81]
	v_mfma_i32_16x16x64_i8 v[74:77], v[130:133], v[212:215], v[74:77]
	v_mfma_i32_16x16x64_i8 v[142:145], v[126:129], v[192:195], v[142:145]
	v_mfma_i32_16x16x64_i8 v[138:141], v[134:137], v[192:195], v[138:141]
	v_mfma_i32_16x16x64_i8 v[110:113], v[126:129], v[200:203], v[110:113]
	v_mfma_i32_16x16x64_i8 v[106:109], v[134:137], v[200:203], v[106:109]
	v_mfma_i32_16x16x64_i8 v[94:97], v[126:129], v[208:211], v[94:97]
	v_mfma_i32_16x16x64_i8 v[90:93], v[134:137], v[208:211], v[90:93]
	v_mfma_i32_16x16x64_i8 v[78:81], v[126:129], v[216:219], v[78:81]
	v_mfma_i32_16x16x64_i8 v[74:77], v[134:137], v[216:219], v[74:77]
	v_mfma_i32_16x16x64_i8 v[118:121], v[172:175], v[188:191], v[118:121]
	v_mfma_i32_16x16x64_i8 v[114:117], v[180:183], v[188:191], v[114:117]
	v_mfma_i32_16x16x64_i8 v[102:105], v[172:175], v[196:199], v[102:105]
	v_mfma_i32_16x16x64_i8 v[98:101], v[180:183], v[196:199], v[98:101]
	v_mfma_i32_16x16x64_i8 v[86:89], v[172:175], v[204:207], v[86:89]
	v_mfma_i32_16x16x64_i8 v[82:85], v[180:183], v[204:207], v[82:85]
	v_mfma_i32_16x16x64_i8 v[70:73], v[172:175], v[212:215], v[70:73]
	v_mfma_i32_16x16x64_i8 v[66:69], v[180:183], v[212:215], v[66:69]
	v_mfma_i32_16x16x64_i8 v[118:121], v[176:179], v[192:195], v[118:121]
	v_mfma_i32_16x16x64_i8 v[114:117], v[184:187], v[192:195], v[114:117]
	v_mfma_i32_16x16x64_i8 v[102:105], v[176:179], v[200:203], v[102:105]
	v_mfma_i32_16x16x64_i8 v[98:101], v[184:187], v[200:203], v[98:101]
	v_mfma_i32_16x16x64_i8 v[86:89], v[176:179], v[208:211], v[86:89]
	v_mfma_i32_16x16x64_i8 v[82:85], v[184:187], v[208:211], v[82:85]
	v_mfma_i32_16x16x64_i8 v[70:73], v[176:179], v[216:219], v[70:73]
	v_mfma_i32_16x16x64_i8 v[66:69], v[184:187], v[216:219], v[66:69]
	s_barrier
	s_add_u32 s98, s26, s10
	s_addc_u32 s99, s27, s11
	s_add_u32 s100, s28, s10
	s_addc_u32 s101, s29, s11
	s_add_i32 s38, s46, s34
	s_mov_b32 m0, s38
	ds_read_b128 v[188:191], v171 offset:16384
	ds_read_b128 v[192:195], v171 offset:17408
	ds_read_b128 v[196:199], v171 offset:18432
	ds_read_b128 v[200:203], v171 offset:19456
	ds_read_b128 v[204:207], v171 offset:20480
	ds_read_b128 v[208:211], v171 offset:21504
	ds_read_b128 v[212:215], v171 offset:22528
	ds_read_b128 v[216:219], v171 offset:23552
	global_load_lds_dwordx4 v148, s[26:27]
	s_add_i32 m0, s38, 0x2000
	s_add_u32 s38, s26, 0x80000
	s_addc_u32 s39, s27, 0
	s_add_i32 s54, s47, s34
	global_load_lds_dwordx4 v152, s[26:27]
	s_mov_b32 m0, s54
	s_nop 0
	global_load_lds_dwordx4 v148, s[38:39]
	s_add_i32 m0, s54, 0x2000
	s_nop 0
	global_load_lds_dwordx4 v152, s[38:39]
	s_mov_b32 m0, s23
	s_nop 0
	global_load_lds_dwordx4 v146, s[28:29]
	s_mov_b32 m0, s35
	s_nop 0
	global_load_lds_dwordx4 v150, s[28:29]
	s_waitcnt vmcnt(8)
	s_waitcnt lgkmcnt(0)
	s_barrier
	v_mfma_i32_16x16x64_i8 v[62:65], v[122:125], v[188:191], v[62:65]
	v_mfma_i32_16x16x64_i8 v[58:61], v[130:133], v[188:191], v[58:61]
	v_mfma_i32_16x16x64_i8 v[46:49], v[122:125], v[196:199], v[46:49]
	v_mfma_i32_16x16x64_i8 v[42:45], v[130:133], v[196:199], v[42:45]
	v_mfma_i32_16x16x64_i8 v[30:33], v[122:125], v[204:207], v[30:33]
	v_mfma_i32_16x16x64_i8 v[26:29], v[130:133], v[204:207], v[26:29]
	v_mfma_i32_16x16x64_i8 v[14:17], v[122:125], v[212:215], v[14:17]
	v_mfma_i32_16x16x64_i8 v[10:13], v[130:133], v[212:215], v[10:13]
	v_mfma_i32_16x16x64_i8 v[62:65], v[126:129], v[192:195], v[62:65]
	v_mfma_i32_16x16x64_i8 v[58:61], v[134:137], v[192:195], v[58:61]
	v_mfma_i32_16x16x64_i8 v[46:49], v[126:129], v[200:203], v[46:49]
	v_mfma_i32_16x16x64_i8 v[42:45], v[134:137], v[200:203], v[42:45]
	v_mfma_i32_16x16x64_i8 v[30:33], v[126:129], v[208:211], v[30:33]
	v_mfma_i32_16x16x64_i8 v[26:29], v[134:137], v[208:211], v[26:29]
	v_mfma_i32_16x16x64_i8 v[14:17], v[126:129], v[216:219], v[14:17]
	v_mfma_i32_16x16x64_i8 v[10:13], v[134:137], v[216:219], v[10:13]
	v_mfma_i32_16x16x64_i8 v[54:57], v[172:175], v[188:191], v[54:57]
	v_mfma_i32_16x16x64_i8 v[50:53], v[180:183], v[188:191], v[50:53]
	v_mfma_i32_16x16x64_i8 v[38:41], v[172:175], v[196:199], v[38:41]
	v_mfma_i32_16x16x64_i8 v[34:37], v[180:183], v[196:199], v[34:37]
	v_mfma_i32_16x16x64_i8 v[22:25], v[172:175], v[204:207], v[22:25]
	v_mfma_i32_16x16x64_i8 v[18:21], v[180:183], v[204:207], v[18:21]
	v_mfma_i32_16x16x64_i8 v[6:9], v[172:175], v[212:215], v[6:9]
	v_mfma_i32_16x16x64_i8 v[2:5], v[180:183], v[212:215], v[2:5]
	v_mfma_i32_16x16x64_i8 v[54:57], v[176:179], v[192:195], v[54:57]
	v_mfma_i32_16x16x64_i8 v[50:53], v[184:187], v[192:195], v[50:53]
	v_mfma_i32_16x16x64_i8 v[38:41], v[176:179], v[200:203], v[38:41]
	v_mfma_i32_16x16x64_i8 v[34:37], v[184:187], v[200:203], v[34:37]
	v_mfma_i32_16x16x64_i8 v[22:25], v[176:179], v[208:211], v[22:25]
	v_mfma_i32_16x16x64_i8 v[18:21], v[184:187], v[208:211], v[18:21]
	v_mfma_i32_16x16x64_i8 v[6:9], v[176:179], v[216:219], v[6:9]
	v_mfma_i32_16x16x64_i8 v[2:5], v[184:187], v[216:219], v[2:5]
	s_barrier
	s_add_i32 s38, 0, 0x18000
	s_add_i32 s39, 0, 0x1c000
	v_add_u32_e32 v134, s38, v167
	v_add_u32_e32 v154, s39, v167
	ds_read_b128 v[122:125], v134
	ds_read_b128 v[126:129], v134 offset:1024
	ds_read_b128 v[130:133], v134 offset:2048
	ds_read_b128 v[134:137], v134 offset:3072
	ds_read_b128 v[172:175], v154
	ds_read_b128 v[176:179], v154 offset:1024
	ds_read_b128 v[180:183], v154 offset:2048
	ds_read_b128 v[184:187], v154 offset:3072
	s_add_u32 s28, s28, 0x80000
	s_addc_u32 s29, s29, 0
	s_mov_b32 m0, s36
	ds_read_b128 v[188:191], v171 offset:32768
	ds_read_b128 v[192:195], v171 offset:33792
	ds_read_b128 v[196:199], v171 offset:34816
	ds_read_b128 v[200:203], v171 offset:35840
	ds_read_b128 v[204:207], v171 offset:36864
	ds_read_b128 v[208:211], v171 offset:37888
	ds_read_b128 v[212:215], v171 offset:38912
	ds_read_b128 v[216:219], v171 offset:39936
	global_load_lds_dwordx4 v146, s[28:29]
	s_mov_b32 m0, s37
	s_nop 0
	global_load_lds_dwordx4 v150, s[28:29]
	s_waitcnt vmcnt(8)
	s_waitcnt lgkmcnt(0)
	s_barrier
	v_mfma_i32_16x16x64_i8 v[142:145], v[122:125], v[188:191], v[142:145]
	v_mfma_i32_16x16x64_i8 v[138:141], v[130:133], v[188:191], v[138:141]
	v_mfma_i32_16x16x64_i8 v[110:113], v[122:125], v[196:199], v[110:113]
	v_mfma_i32_16x16x64_i8 v[106:109], v[130:133], v[196:199], v[106:109]
	v_mfma_i32_16x16x64_i8 v[94:97], v[122:125], v[204:207], v[94:97]
	v_mfma_i32_16x16x64_i8 v[90:93], v[130:133], v[204:207], v[90:93]
	v_mfma_i32_16x16x64_i8 v[78:81], v[122:125], v[212:215], v[78:81]
	v_mfma_i32_16x16x64_i8 v[74:77], v[130:133], v[212:215], v[74:77]
	v_mfma_i32_16x16x64_i8 v[142:145], v[126:129], v[192:195], v[142:145]
	v_mfma_i32_16x16x64_i8 v[138:141], v[134:137], v[192:195], v[138:141]
	v_mfma_i32_16x16x64_i8 v[110:113], v[126:129], v[200:203], v[110:113]
	v_mfma_i32_16x16x64_i8 v[106:109], v[134:137], v[200:203], v[106:109]
	v_mfma_i32_16x16x64_i8 v[94:97], v[126:129], v[208:211], v[94:97]
	v_mfma_i32_16x16x64_i8 v[90:93], v[134:137], v[208:211], v[90:93]
	v_mfma_i32_16x16x64_i8 v[78:81], v[126:129], v[216:219], v[78:81]
	v_mfma_i32_16x16x64_i8 v[74:77], v[134:137], v[216:219], v[74:77]
	v_mfma_i32_16x16x64_i8 v[118:121], v[172:175], v[188:191], v[118:121]
	v_mfma_i32_16x16x64_i8 v[114:117], v[180:183], v[188:191], v[114:117]
	v_mfma_i32_16x16x64_i8 v[102:105], v[172:175], v[196:199], v[102:105]
	v_mfma_i32_16x16x64_i8 v[98:101], v[180:183], v[196:199], v[98:101]
	v_mfma_i32_16x16x64_i8 v[86:89], v[172:175], v[204:207], v[86:89]
	v_mfma_i32_16x16x64_i8 v[82:85], v[180:183], v[204:207], v[82:85]
	v_mfma_i32_16x16x64_i8 v[70:73], v[172:175], v[212:215], v[70:73]
	v_mfma_i32_16x16x64_i8 v[66:69], v[180:183], v[212:215], v[66:69]
	v_mfma_i32_16x16x64_i8 v[118:121], v[176:179], v[192:195], v[118:121]
	v_mfma_i32_16x16x64_i8 v[114:117], v[184:187], v[192:195], v[114:117]
	v_mfma_i32_16x16x64_i8 v[102:105], v[176:179], v[200:203], v[102:105]
	v_mfma_i32_16x16x64_i8 v[98:101], v[184:187], v[200:203], v[98:101]
	v_mfma_i32_16x16x64_i8 v[86:89], v[176:179], v[208:211], v[86:89]
	v_mfma_i32_16x16x64_i8 v[82:85], v[184:187], v[208:211], v[82:85]
	v_mfma_i32_16x16x64_i8 v[70:73], v[176:179], v[216:219], v[70:73]
	v_mfma_i32_16x16x64_i8 v[66:69], v[184:187], v[216:219], v[66:69]
	s_barrier
	s_add_i32 s28, s38, s34
	s_mov_b32 m0, s28
	ds_read_b128 v[188:191], v171 offset:49152
	ds_read_b128 v[192:195], v171 offset:50176
	ds_read_b128 v[196:199], v171 offset:51200
	ds_read_b128 v[200:203], v171 offset:52224
	ds_read_b128 v[204:207], v171 offset:53248
	ds_read_b128 v[208:211], v171 offset:54272
	ds_read_b128 v[212:215], v171 offset:55296
	ds_read_b128 v[216:219], v171 offset:56320
	global_load_lds_dwordx4 v148, s[98:99]
	s_add_i32 m0, s28, 0x2000
	s_add_u32 s26, s26, 0x80080
	s_addc_u32 s27, s27, 0
	s_add_i32 s28, s39, s34
	global_load_lds_dwordx4 v152, s[98:99]
	s_mov_b32 m0, s28
	s_nop 0
	global_load_lds_dwordx4 v148, s[26:27]
	s_add_i32 m0, s28, 0x2000
	s_nop 0
	global_load_lds_dwordx4 v152, s[26:27]
	s_mov_b32 m0, s43
	s_nop 0
	global_load_lds_dwordx4 v146, s[100:101]
	s_mov_b32 m0, s44
	s_nop 0
	global_load_lds_dwordx4 v150, s[100:101]
	s_waitcnt vmcnt(8)
	s_waitcnt lgkmcnt(0)
	s_barrier
	v_mfma_i32_16x16x64_i8 v[62:65], v[122:125], v[188:191], v[62:65]
	v_mfma_i32_16x16x64_i8 v[58:61], v[130:133], v[188:191], v[58:61]
	v_mfma_i32_16x16x64_i8 v[46:49], v[122:125], v[196:199], v[46:49]
	v_mfma_i32_16x16x64_i8 v[42:45], v[130:133], v[196:199], v[42:45]
	v_mfma_i32_16x16x64_i8 v[30:33], v[122:125], v[204:207], v[30:33]
	v_mfma_i32_16x16x64_i8 v[26:29], v[130:133], v[204:207], v[26:29]
	v_mfma_i32_16x16x64_i8 v[14:17], v[122:125], v[212:215], v[14:17]
	v_mfma_i32_16x16x64_i8 v[10:13], v[130:133], v[212:215], v[10:13]
	v_mfma_i32_16x16x64_i8 v[62:65], v[126:129], v[192:195], v[62:65]
	v_mfma_i32_16x16x64_i8 v[58:61], v[134:137], v[192:195], v[58:61]
	v_mfma_i32_16x16x64_i8 v[46:49], v[126:129], v[200:203], v[46:49]
	v_mfma_i32_16x16x64_i8 v[42:45], v[134:137], v[200:203], v[42:45]
	v_mfma_i32_16x16x64_i8 v[30:33], v[126:129], v[208:211], v[30:33]
	v_mfma_i32_16x16x64_i8 v[26:29], v[134:137], v[208:211], v[26:29]
	v_mfma_i32_16x16x64_i8 v[14:17], v[126:129], v[216:219], v[14:17]
	v_mfma_i32_16x16x64_i8 v[10:13], v[134:137], v[216:219], v[10:13]
	v_mfma_i32_16x16x64_i8 v[54:57], v[172:175], v[188:191], v[54:57]
	v_mfma_i32_16x16x64_i8 v[50:53], v[180:183], v[188:191], v[50:53]
	v_mfma_i32_16x16x64_i8 v[38:41], v[172:175], v[196:199], v[38:41]
	v_mfma_i32_16x16x64_i8 v[34:37], v[180:183], v[196:199], v[34:37]
	v_mfma_i32_16x16x64_i8 v[22:25], v[172:175], v[204:207], v[22:25]
	v_mfma_i32_16x16x64_i8 v[18:21], v[180:183], v[204:207], v[18:21]
	v_mfma_i32_16x16x64_i8 v[6:9], v[172:175], v[212:215], v[6:9]
	v_mfma_i32_16x16x64_i8 v[2:5], v[180:183], v[212:215], v[2:5]
	v_mfma_i32_16x16x64_i8 v[54:57], v[176:179], v[192:195], v[54:57]
	v_mfma_i32_16x16x64_i8 v[50:53], v[184:187], v[192:195], v[50:53]
	v_mfma_i32_16x16x64_i8 v[38:41], v[176:179], v[200:203], v[38:41]
	v_mfma_i32_16x16x64_i8 v[34:37], v[184:187], v[200:203], v[34:37]
	v_mfma_i32_16x16x64_i8 v[22:25], v[176:179], v[208:211], v[22:25]
	v_mfma_i32_16x16x64_i8 v[18:21], v[184:187], v[208:211], v[18:21]
	v_mfma_i32_16x16x64_i8 v[6:9], v[176:179], v[216:219], v[6:9]
	v_mfma_i32_16x16x64_i8 v[2:5], v[184:187], v[216:219], v[2:5]
	s_barrier
	s_add_i32 s53, s53, 2
	s_add_u32 s24, s24, 0x100
	s_addc_u32 s25, s25, 0
	s_add_u32 s51, s51, 0x100
	s_addc_u32 s52, s52, 0
	s_cmp_gt_u32 s53, 29
	s_cbranch_scc0 .LBB0_1489
	s_setprio 0
	s_and_b64 vcc, exec, s[12:13]
	s_cbranch_vccz .LBB0_1492
	s_barrier

.Lprio_P8:
.LBB0_1649:
	ds_read_b128 v[130:133], v167
	ds_read_b128 v[134:137], v167 offset:1024
	ds_read_b128 v[138:141], v167 offset:2048
	ds_read_b128 v[142:145], v167 offset:3072
	ds_read_b128 v[168:171], v228
	ds_read_b128 v[172:175], v228 offset:1024
	ds_read_b128 v[176:179], v228 offset:2048
	ds_read_b128 v[180:183], v228 offset:3072
	s_add_u32 s38, s34, 0xfff80080
	s_addc_u32 s39, s35, -1
	s_cmp_eq_u32 s77, 28
	s_cselect_b32 s45, s1, s39
	s_cselect_b32 s44, s29, s38
	s_cselect_b32 s43, s27, s47
	s_cselect_b32 s42, s41, s46
	s_add_i32 m0, s50, 0xc000
	ds_read_b128 v[184:187], v229
	ds_read_b128 v[188:191], v229 offset:1024
	ds_read_b128 v[192:195], v229 offset:2048
	ds_read_b128 v[196:199], v229 offset:3072
	ds_read_b128 v[200:203], v229 offset:4096
	ds_read_b128 v[204:207], v229 offset:5120
	ds_read_b128 v[208:211], v229 offset:6144
	ds_read_b128 v[212:215], v229 offset:7168
	global_load_lds_dwordx4 v158, s[34:35]
	s_add_i32 m0, s50, 0xe000
	s_nop 0
	global_load_lds_dwordx4 v160, s[34:35]
	s_waitcnt vmcnt(8)
	s_waitcnt lgkmcnt(0)
	s_barrier
	v_mfma_i32_16x16x64_i8 v[46:49], v[130:133], v[184:187], v[46:49]
	v_mfma_i32_16x16x64_i8 v[34:37], v[138:141], v[184:187], v[34:37]
	v_mfma_i32_16x16x64_i8 v[42:45], v[130:133], v[192:195], v[42:45]
	v_mfma_i32_16x16x64_i8 v[30:33], v[138:141], v[192:195], v[30:33]
	v_mfma_i32_16x16x64_i8 v[38:41], v[130:133], v[200:203], v[38:41]
	v_mfma_i32_16x16x64_i8 v[26:29], v[138:141], v[200:203], v[26:29]
	v_mfma_i32_16x16x64_i8 v[126:129], v[130:133], v[208:211], v[126:129]
	v_mfma_i32_16x16x64_i8 v[122:125], v[138:141], v[208:211], v[122:125]
	v_mfma_i32_16x16x64_i8 v[46:49], v[134:137], v[188:191], v[46:49]
	v_mfma_i32_16x16x64_i8 v[34:37], v[142:145], v[188:191], v[34:37]
	v_mfma_i32_16x16x64_i8 v[42:45], v[134:137], v[196:199], v[42:45]
	v_mfma_i32_16x16x64_i8 v[30:33], v[142:145], v[196:199], v[30:33]
	v_mfma_i32_16x16x64_i8 v[38:41], v[134:137], v[204:207], v[38:41]
	v_mfma_i32_16x16x64_i8 v[26:29], v[142:145], v[204:207], v[26:29]
	v_mfma_i32_16x16x64_i8 v[126:129], v[134:137], v[212:215], v[126:129]
	v_mfma_i32_16x16x64_i8 v[122:125], v[142:145], v[212:215], v[122:125]
	v_mfma_i32_16x16x64_i8 v[22:25], v[168:171], v[184:187], v[22:25]
	v_mfma_i32_16x16x64_i8 v[10:13], v[176:179], v[184:187], v[10:13]
	v_mfma_i32_16x16x64_i8 v[18:21], v[168:171], v[192:195], v[18:21]
	v_mfma_i32_16x16x64_i8 v[6:9], v[176:179], v[192:195], v[6:9]
	v_mfma_i32_16x16x64_i8 v[14:17], v[168:171], v[200:203], v[14:17]
	v_mfma_i32_16x16x64_i8 v[2:5], v[176:179], v[200:203], v[2:5]
	v_mfma_i32_16x16x64_i8 v[118:121], v[168:171], v[208:211], v[118:121]
	v_mfma_i32_16x16x64_i8 v[114:117], v[176:179], v[208:211], v[114:117]
	v_mfma_i32_16x16x64_i8 v[22:25], v[172:175], v[188:191], v[22:25]
	v_mfma_i32_16x16x64_i8 v[10:13], v[180:183], v[188:191], v[10:13]
	v_mfma_i32_16x16x64_i8 v[18:21], v[172:175], v[196:199], v[18:21]
	v_mfma_i32_16x16x64_i8 v[6:9], v[180:183], v[196:199], v[6:9]
	v_mfma_i32_16x16x64_i8 v[14:17], v[172:175], v[204:207], v[14:17]
	v_mfma_i32_16x16x64_i8 v[2:5], v[180:183], v[204:207], v[2:5]
	v_mfma_i32_16x16x64_i8 v[118:121], v[172:175], v[212:215], v[118:121]
	v_mfma_i32_16x16x64_i8 v[114:117], v[180:183], v[212:215], v[114:117]
	s_barrier
	s_add_u32 s98, s42, s14
	s_addc_u32 s99, s43, s15
	s_add_u32 s100, s44, s14
	s_addc_u32 s101, s45, s15
	s_add_i32 s38, s64, s49
	s_mov_b32 m0, s38
	ds_read_b128 v[184:187], v229 offset:16384
	ds_read_b128 v[188:191], v229 offset:17408
	ds_read_b128 v[192:195], v229 offset:18432
	ds_read_b128 v[196:199], v229 offset:19456
	ds_read_b128 v[200:203], v229 offset:20480
	ds_read_b128 v[204:207], v229 offset:21504
	ds_read_b128 v[208:211], v229 offset:22528
	ds_read_b128 v[212:215], v229 offset:23552
	global_load_lds_dwordx4 v150, s[42:43]
	s_add_i32 m0, s38, 0x2000
	s_add_u32 s38, s42, 0x80000
	s_addc_u32 s39, s43, 0
	s_add_i32 s78, s65, s49
	global_load_lds_dwordx4 v154, s[42:43]
	s_mov_b32 m0, s78
	s_nop 0
	global_load_lds_dwordx4 v150, s[38:39]
	s_add_i32 m0, s78, 0x2000
	s_nop 0
	global_load_lds_dwordx4 v154, s[38:39]
	s_mov_b32 m0, s50
	s_nop 0
	global_load_lds_dwordx4 v148, s[44:45]
	s_mov_b32 m0, s51
	s_nop 0
	global_load_lds_dwordx4 v152, s[44:45]
	s_waitcnt vmcnt(8)
	s_waitcnt lgkmcnt(0)
	s_barrier
	v_mfma_i32_16x16x64_i8 v[94:97], v[130:133], v[184:187], v[94:97]
	v_mfma_i32_16x16x64_i8 v[70:73], v[138:141], v[184:187], v[70:73]
	v_mfma_i32_16x16x64_i8 v[86:89], v[130:133], v[192:195], v[86:89]
	v_mfma_i32_16x16x64_i8 v[62:65], v[138:141], v[192:195], v[62:65]
	v_mfma_i32_16x16x64_i8 v[78:81], v[130:133], v[200:203], v[78:81]
	v_mfma_i32_16x16x64_i8 v[54:57], v[138:141], v[200:203], v[54:57]
	v_mfma_i32_16x16x64_i8 v[110:113], v[130:133], v[208:211], v[110:113]
	v_mfma_i32_16x16x64_i8 v[106:109], v[138:141], v[208:211], v[106:109]
	v_mfma_i32_16x16x64_i8 v[94:97], v[134:137], v[188:191], v[94:97]
	v_mfma_i32_16x16x64_i8 v[70:73], v[142:145], v[188:191], v[70:73]
	v_mfma_i32_16x16x64_i8 v[86:89], v[134:137], v[196:199], v[86:89]
	v_mfma_i32_16x16x64_i8 v[62:65], v[142:145], v[196:199], v[62:65]
	v_mfma_i32_16x16x64_i8 v[78:81], v[134:137], v[204:207], v[78:81]
	v_mfma_i32_16x16x64_i8 v[54:57], v[142:145], v[204:207], v[54:57]
	v_mfma_i32_16x16x64_i8 v[110:113], v[134:137], v[212:215], v[110:113]
	v_mfma_i32_16x16x64_i8 v[106:109], v[142:145], v[212:215], v[106:109]
	v_mfma_i32_16x16x64_i8 v[90:93], v[168:171], v[184:187], v[90:93]
	v_mfma_i32_16x16x64_i8 v[66:69], v[176:179], v[184:187], v[66:69]
	v_mfma_i32_16x16x64_i8 v[82:85], v[168:171], v[192:195], v[82:85]
	v_mfma_i32_16x16x64_i8 v[58:61], v[176:179], v[192:195], v[58:61]
	v_mfma_i32_16x16x64_i8 v[74:77], v[168:171], v[200:203], v[74:77]
	v_mfma_i32_16x16x64_i8 v[50:53], v[176:179], v[200:203], v[50:53]
	v_mfma_i32_16x16x64_i8 v[102:105], v[168:171], v[208:211], v[102:105]
	v_mfma_i32_16x16x64_i8 v[98:101], v[176:179], v[208:211], v[98:101]
	v_mfma_i32_16x16x64_i8 v[90:93], v[172:175], v[188:191], v[90:93]
	v_mfma_i32_16x16x64_i8 v[66:69], v[180:183], v[188:191], v[66:69]
	v_mfma_i32_16x16x64_i8 v[82:85], v[172:175], v[196:199], v[82:85]
	v_mfma_i32_16x16x64_i8 v[58:61], v[180:183], v[196:199], v[58:61]
	v_mfma_i32_16x16x64_i8 v[74:77], v[172:175], v[204:207], v[74:77]
	v_mfma_i32_16x16x64_i8 v[50:53], v[180:183], v[204:207], v[50:53]
	v_mfma_i32_16x16x64_i8 v[102:105], v[172:175], v[212:215], v[102:105]
	v_mfma_i32_16x16x64_i8 v[98:101], v[180:183], v[212:215], v[98:101]
	s_barrier
	s_add_i32 s78, 0, 0x18000
	s_add_i32 s79, 0, 0x1c000
	v_add_u32_e32 v142, s78, v1
	v_add_u32_e32 v156, s79, v1
	ds_read_b128 v[130:133], v142
	ds_read_b128 v[134:137], v142 offset:1024
	ds_read_b128 v[138:141], v142 offset:2048
	ds_read_b128 v[142:145], v142 offset:3072
	ds_read_b128 v[168:171], v156
	ds_read_b128 v[172:175], v156 offset:1024
	ds_read_b128 v[176:179], v156 offset:2048
	ds_read_b128 v[180:183], v156 offset:3072
	s_add_u32 s38, s44, 0x80000
	s_addc_u32 s39, s45, 0
	s_mov_b32 m0, s52
	ds_read_b128 v[184:187], v229 offset:32768
	ds_read_b128 v[188:191], v229 offset:33792
	ds_read_b128 v[192:195], v229 offset:34816
	ds_read_b128 v[196:199], v229 offset:35840
	ds_read_b128 v[200:203], v229 offset:36864
	ds_read_b128 v[204:207], v229 offset:37888
	ds_read_b128 v[208:211], v229 offset:38912
	ds_read_b128 v[212:215], v229 offset:39936
	global_load_lds_dwordx4 v148, s[38:39]
	s_mov_b32 m0, s53
	s_nop 0
	global_load_lds_dwordx4 v152, s[38:39]
	s_waitcnt vmcnt(8)
	s_waitcnt lgkmcnt(0)
	s_barrier
	v_mfma_i32_16x16x64_i8 v[46:49], v[130:133], v[184:187], v[46:49]
	v_mfma_i32_16x16x64_i8 v[34:37], v[138:141], v[184:187], v[34:37]
	v_mfma_i32_16x16x64_i8 v[42:45], v[130:133], v[192:195], v[42:45]
	v_mfma_i32_16x16x64_i8 v[30:33], v[138:141], v[192:195], v[30:33]
	v_mfma_i32_16x16x64_i8 v[38:41], v[130:133], v[200:203], v[38:41]
	v_mfma_i32_16x16x64_i8 v[26:29], v[138:141], v[200:203], v[26:29]
	v_mfma_i32_16x16x64_i8 v[126:129], v[130:133], v[208:211], v[126:129]
	v_mfma_i32_16x16x64_i8 v[122:125], v[138:141], v[208:211], v[122:125]
	v_mfma_i32_16x16x64_i8 v[46:49], v[134:137], v[188:191], v[46:49]
	v_mfma_i32_16x16x64_i8 v[34:37], v[142:145], v[188:191], v[34:37]
	v_mfma_i32_16x16x64_i8 v[42:45], v[134:137], v[196:199], v[42:45]
	v_mfma_i32_16x16x64_i8 v[30:33], v[142:145], v[196:199], v[30:33]
	v_mfma_i32_16x16x64_i8 v[38:41], v[134:137], v[204:207], v[38:41]
	v_mfma_i32_16x16x64_i8 v[26:29], v[142:145], v[204:207], v[26:29]
	v_mfma_i32_16x16x64_i8 v[126:129], v[134:137], v[212:215], v[126:129]
	v_mfma_i32_16x16x64_i8 v[122:125], v[142:145], v[212:215], v[122:125]
	v_mfma_i32_16x16x64_i8 v[22:25], v[168:171], v[184:187], v[22:25]
	v_mfma_i32_16x16x64_i8 v[10:13], v[176:179], v[184:187], v[10:13]
	v_mfma_i32_16x16x64_i8 v[18:21], v[168:171], v[192:195], v[18:21]
	v_mfma_i32_16x16x64_i8 v[6:9], v[176:179], v[192:195], v[6:9]
	v_mfma_i32_16x16x64_i8 v[14:17], v[168:171], v[200:203], v[14:17]
	v_mfma_i32_16x16x64_i8 v[2:5], v[176:179], v[200:203], v[2:5]
	v_mfma_i32_16x16x64_i8 v[118:121], v[168:171], v[208:211], v[118:121]
	v_mfma_i32_16x16x64_i8 v[114:117], v[176:179], v[208:211], v[114:117]
	v_mfma_i32_16x16x64_i8 v[22:25], v[172:175], v[188:191], v[22:25]
	v_mfma_i32_16x16x64_i8 v[10:13], v[180:183], v[188:191], v[10:13]
	v_mfma_i32_16x16x64_i8 v[18:21], v[172:175], v[196:199], v[18:21]
	v_mfma_i32_16x16x64_i8 v[6:9], v[180:183], v[196:199], v[6:9]
	v_mfma_i32_16x16x64_i8 v[14:17], v[172:175], v[204:207], v[14:17]
	v_mfma_i32_16x16x64_i8 v[2:5], v[180:183], v[204:207], v[2:5]
	v_mfma_i32_16x16x64_i8 v[118:121], v[172:175], v[212:215], v[118:121]
	v_mfma_i32_16x16x64_i8 v[114:117], v[180:183], v[212:215], v[114:117]
	s_barrier
	s_add_i32 s38, s78, s49
	s_mov_b32 m0, s38
	ds_read_b128 v[184:187], v229 offset:49152
	ds_read_b128 v[188:191], v229 offset:50176
	ds_read_b128 v[192:195], v229 offset:51200
	ds_read_b128 v[196:199], v229 offset:52224
	ds_read_b128 v[200:203], v229 offset:53248
	ds_read_b128 v[204:207], v229 offset:54272
	ds_read_b128 v[208:211], v229 offset:55296
	ds_read_b128 v[212:215], v229 offset:56320
	global_load_lds_dwordx4 v150, s[98:99]
	s_add_i32 m0, s38, 0x2000
	s_add_u32 s38, s42, 0x80080
	s_addc_u32 s39, s43, 0
	s_add_i32 s42, s79, s49
	global_load_lds_dwordx4 v154, s[98:99]
	s_mov_b32 m0, s42
	s_nop 0
	global_load_lds_dwordx4 v150, s[38:39]
	s_add_i32 m0, s42, 0x2000
	s_nop 0
	global_load_lds_dwordx4 v154, s[38:39]
	s_mov_b32 m0, s57
	s_nop 0
	global_load_lds_dwordx4 v148, s[100:101]
	s_mov_b32 m0, s58
	s_nop 0
	global_load_lds_dwordx4 v152, s[100:101]
	s_waitcnt vmcnt(8)
	s_waitcnt lgkmcnt(0)
	s_barrier
	v_mfma_i32_16x16x64_i8 v[94:97], v[130:133], v[184:187], v[94:97]
	v_mfma_i32_16x16x64_i8 v[70:73], v[138:141], v[184:187], v[70:73]
	v_mfma_i32_16x16x64_i8 v[86:89], v[130:133], v[192:195], v[86:89]
	v_mfma_i32_16x16x64_i8 v[62:65], v[138:141], v[192:195], v[62:65]
	v_mfma_i32_16x16x64_i8 v[78:81], v[130:133], v[200:203], v[78:81]
	v_mfma_i32_16x16x64_i8 v[54:57], v[138:141], v[200:203], v[54:57]
	v_mfma_i32_16x16x64_i8 v[110:113], v[130:133], v[208:211], v[110:113]
	v_mfma_i32_16x16x64_i8 v[106:109], v[138:141], v[208:211], v[106:109]
	v_mfma_i32_16x16x64_i8 v[94:97], v[134:137], v[188:191], v[94:97]
	v_mfma_i32_16x16x64_i8 v[70:73], v[142:145], v[188:191], v[70:73]
	v_mfma_i32_16x16x64_i8 v[86:89], v[134:137], v[196:199], v[86:89]
	v_mfma_i32_16x16x64_i8 v[62:65], v[142:145], v[196:199], v[62:65]
	v_mfma_i32_16x16x64_i8 v[78:81], v[134:137], v[204:207], v[78:81]
	v_mfma_i32_16x16x64_i8 v[54:57], v[142:145], v[204:207], v[54:57]
	v_mfma_i32_16x16x64_i8 v[110:113], v[134:137], v[212:215], v[110:113]
	v_mfma_i32_16x16x64_i8 v[106:109], v[142:145], v[212:215], v[106:109]
	v_mfma_i32_16x16x64_i8 v[90:93], v[168:171], v[184:187], v[90:93]
	v_mfma_i32_16x16x64_i8 v[66:69], v[176:179], v[184:187], v[66:69]
	v_mfma_i32_16x16x64_i8 v[82:85], v[168:171], v[192:195], v[82:85]
	v_mfma_i32_16x16x64_i8 v[58:61], v[176:179], v[192:195], v[58:61]
	v_mfma_i32_16x16x64_i8 v[74:77], v[168:171], v[200:203], v[74:77]
	v_mfma_i32_16x16x64_i8 v[50:53], v[176:179], v[200:203], v[50:53]
	v_mfma_i32_16x16x64_i8 v[102:105], v[168:171], v[208:211], v[102:105]
	v_mfma_i32_16x16x64_i8 v[98:101], v[176:179], v[208:211], v[98:101]
	v_mfma_i32_16x16x64_i8 v[90:93], v[172:175], v[188:191], v[90:93]
	v_mfma_i32_16x16x64_i8 v[66:69], v[180:183], v[188:191], v[66:69]
	v_mfma_i32_16x16x64_i8 v[82:85], v[172:175], v[196:199], v[82:85]
	v_mfma_i32_16x16x64_i8 v[58:61], v[180:183], v[196:199], v[58:61]
	v_mfma_i32_16x16x64_i8 v[74:77], v[172:175], v[204:207], v[74:77]
	v_mfma_i32_16x16x64_i8 v[50:53], v[180:183], v[204:207], v[50:53]
	v_mfma_i32_16x16x64_i8 v[102:105], v[172:175], v[212:215], v[102:105]
	v_mfma_i32_16x16x64_i8 v[98:101], v[180:183], v[212:215], v[98:101]
	s_barrier
	s_add_i32 s77, s77, 2
	s_add_u32 s34, s34, 0x100
	s_addc_u32 s35, s35, 0
	s_add_u32 s46, s46, 0x100
	s_addc_u32 s47, s47, 0
	s_cmp_gt_u32 s77, 29
	s_cbranch_scc0 .LBB0_1649
	s_setprio 0
	s_and_b64 vcc, exec, s[16:17]
	s_cbranch_vccz .LBB0_1652
	s_barrier

.Lprio_P10:
.LBB0_1899:
	ds_read_b128 v[122:125], v169
	ds_read_b128 v[126:129], v169 offset:1024
	ds_read_b128 v[130:133], v169 offset:2048
	ds_read_b128 v[134:137], v169 offset:3072
	ds_read_b128 v[172:175], v170
	ds_read_b128 v[176:179], v170 offset:1024
	ds_read_b128 v[180:183], v170 offset:2048
	ds_read_b128 v[184:187], v170 offset:3072
	s_add_u32 s22, s20, 0xffea8080
	s_addc_u32 s23, s21, -1
	s_cmpk_eq_i32 s49, 0x52
	s_cselect_b32 s25, s5, s23
	s_cselect_b32 s24, s4, s22
	s_cselect_b32 s23, s19, s48
	s_cselect_b32 s22, s18, s47
	s_add_i32 m0, s30, 0xc000
	ds_read_b128 v[188:191], v171
	ds_read_b128 v[192:195], v171 offset:1024
	ds_read_b128 v[196:199], v171 offset:2048
	ds_read_b128 v[200:203], v171 offset:3072
	ds_read_b128 v[204:207], v171 offset:4096
	ds_read_b128 v[208:211], v171 offset:5120
	ds_read_b128 v[212:215], v171 offset:6144
	ds_read_b128 v[216:219], v171 offset:7168
	global_load_lds_dwordx4 v156, s[20:21]
	s_add_i32 m0, s30, 0xe000
	s_nop 0
	global_load_lds_dwordx4 v158, s[20:21]
	s_waitcnt vmcnt(8)
	s_waitcnt lgkmcnt(0)
	s_barrier
	v_mfma_i32_16x16x64_i8 v[142:145], v[122:125], v[188:191], v[142:145]
	v_mfma_i32_16x16x64_i8 v[138:141], v[130:133], v[188:191], v[138:141]
	v_mfma_i32_16x16x64_i8 v[110:113], v[122:125], v[196:199], v[110:113]
	v_mfma_i32_16x16x64_i8 v[106:109], v[130:133], v[196:199], v[106:109]
	v_mfma_i32_16x16x64_i8 v[94:97], v[122:125], v[204:207], v[94:97]
	v_mfma_i32_16x16x64_i8 v[90:93], v[130:133], v[204:207], v[90:93]
	v_mfma_i32_16x16x64_i8 v[78:81], v[122:125], v[212:215], v[78:81]
	v_mfma_i32_16x16x64_i8 v[74:77], v[130:133], v[212:215], v[74:77]
	v_mfma_i32_16x16x64_i8 v[142:145], v[126:129], v[192:195], v[142:145]
	v_mfma_i32_16x16x64_i8 v[138:141], v[134:137], v[192:195], v[138:141]
	v_mfma_i32_16x16x64_i8 v[110:113], v[126:129], v[200:203], v[110:113]
	v_mfma_i32_16x16x64_i8 v[106:109], v[134:137], v[200:203], v[106:109]
	v_mfma_i32_16x16x64_i8 v[94:97], v[126:129], v[208:211], v[94:97]
	v_mfma_i32_16x16x64_i8 v[90:93], v[134:137], v[208:211], v[90:93]
	v_mfma_i32_16x16x64_i8 v[78:81], v[126:129], v[216:219], v[78:81]
	v_mfma_i32_16x16x64_i8 v[74:77], v[134:137], v[216:219], v[74:77]
	v_mfma_i32_16x16x64_i8 v[118:121], v[172:175], v[188:191], v[118:121]
	v_mfma_i32_16x16x64_i8 v[114:117], v[180:183], v[188:191], v[114:117]
	v_mfma_i32_16x16x64_i8 v[102:105], v[172:175], v[196:199], v[102:105]
	v_mfma_i32_16x16x64_i8 v[98:101], v[180:183], v[196:199], v[98:101]
	v_mfma_i32_16x16x64_i8 v[86:89], v[172:175], v[204:207], v[86:89]
	v_mfma_i32_16x16x64_i8 v[82:85], v[180:183], v[204:207], v[82:85]
	v_mfma_i32_16x16x64_i8 v[70:73], v[172:175], v[212:215], v[70:73]
	v_mfma_i32_16x16x64_i8 v[66:69], v[180:183], v[212:215], v[66:69]
	v_mfma_i32_16x16x64_i8 v[118:121], v[176:179], v[192:195], v[118:121]
	v_mfma_i32_16x16x64_i8 v[114:117], v[184:187], v[192:195], v[114:117]
	v_mfma_i32_16x16x64_i8 v[102:105], v[176:179], v[200:203], v[102:105]
	v_mfma_i32_16x16x64_i8 v[98:101], v[184:187], v[200:203], v[98:101]
	v_mfma_i32_16x16x64_i8 v[86:89], v[176:179], v[208:211], v[86:89]
	v_mfma_i32_16x16x64_i8 v[82:85], v[184:187], v[208:211], v[82:85]
	v_mfma_i32_16x16x64_i8 v[70:73], v[176:179], v[216:219], v[70:73]
	v_mfma_i32_16x16x64_i8 v[66:69], v[184:187], v[216:219], v[66:69]
	s_barrier
	s_add_u32 s98, s22, s14
	s_addc_u32 s99, s23, s15
	s_add_u32 s100, s24, s14
	s_addc_u32 s101, s25, s15
	s_add_i32 s38, s41, s29
	s_mov_b32 m0, s38
	ds_read_b128 v[188:191], v171 offset:16384
	ds_read_b128 v[192:195], v171 offset:17408
	ds_read_b128 v[196:199], v171 offset:18432
	ds_read_b128 v[200:203], v171 offset:19456
	ds_read_b128 v[204:207], v171 offset:20480
	ds_read_b128 v[208:211], v171 offset:21504
	ds_read_b128 v[212:215], v171 offset:22528
	ds_read_b128 v[216:219], v171 offset:23552
	global_load_lds_dwordx4 v148, s[22:23]
	s_add_i32 m0, s38, 0x2000
	s_add_u32 s38, s22, 0x158000
	s_addc_u32 s39, s23, 0
	s_add_i32 s50, s42, s29
	global_load_lds_dwordx4 v152, s[22:23]
	s_mov_b32 m0, s50
	s_nop 0
	global_load_lds_dwordx4 v148, s[38:39]
	s_add_i32 m0, s50, 0x2000
	s_nop 0
	global_load_lds_dwordx4 v152, s[38:39]
	s_mov_b32 m0, s30
	s_nop 0
	global_load_lds_dwordx4 v146, s[24:25]
	s_mov_b32 m0, s31
	s_nop 0
	global_load_lds_dwordx4 v150, s[24:25]
	s_waitcnt vmcnt(8)
	s_waitcnt lgkmcnt(0)
	s_barrier
	v_mfma_i32_16x16x64_i8 v[62:65], v[122:125], v[188:191], v[62:65]
	v_mfma_i32_16x16x64_i8 v[58:61], v[130:133], v[188:191], v[58:61]
	v_mfma_i32_16x16x64_i8 v[46:49], v[122:125], v[196:199], v[46:49]
	v_mfma_i32_16x16x64_i8 v[42:45], v[130:133], v[196:199], v[42:45]
	v_mfma_i32_16x16x64_i8 v[30:33], v[122:125], v[204:207], v[30:33]
	v_mfma_i32_16x16x64_i8 v[26:29], v[130:133], v[204:207], v[26:29]
	v_mfma_i32_16x16x64_i8 v[14:17], v[122:125], v[212:215], v[14:17]
	v_mfma_i32_16x16x64_i8 v[10:13], v[130:133], v[212:215], v[10:13]
	v_mfma_i32_16x16x64_i8 v[62:65], v[126:129], v[192:195], v[62:65]
	v_mfma_i32_16x16x64_i8 v[58:61], v[134:137], v[192:195], v[58:61]
	v_mfma_i32_16x16x64_i8 v[46:49], v[126:129], v[200:203], v[46:49]
	v_mfma_i32_16x16x64_i8 v[42:45], v[134:137], v[200:203], v[42:45]
	v_mfma_i32_16x16x64_i8 v[30:33], v[126:129], v[208:211], v[30:33]
	v_mfma_i32_16x16x64_i8 v[26:29], v[134:137], v[208:211], v[26:29]
	v_mfma_i32_16x16x64_i8 v[14:17], v[126:129], v[216:219], v[14:17]
	v_mfma_i32_16x16x64_i8 v[10:13], v[134:137], v[216:219], v[10:13]
	v_mfma_i32_16x16x64_i8 v[54:57], v[172:175], v[188:191], v[54:57]
	v_mfma_i32_16x16x64_i8 v[50:53], v[180:183], v[188:191], v[50:53]
	v_mfma_i32_16x16x64_i8 v[38:41], v[172:175], v[196:199], v[38:41]
	v_mfma_i32_16x16x64_i8 v[34:37], v[180:183], v[196:199], v[34:37]
	v_mfma_i32_16x16x64_i8 v[22:25], v[172:175], v[204:207], v[22:25]
	v_mfma_i32_16x16x64_i8 v[18:21], v[180:183], v[204:207], v[18:21]
	v_mfma_i32_16x16x64_i8 v[6:9], v[172:175], v[212:215], v[6:9]
	v_mfma_i32_16x16x64_i8 v[2:5], v[180:183], v[212:215], v[2:5]
	v_mfma_i32_16x16x64_i8 v[54:57], v[176:179], v[192:195], v[54:57]
	v_mfma_i32_16x16x64_i8 v[50:53], v[184:187], v[192:195], v[50:53]
	v_mfma_i32_16x16x64_i8 v[38:41], v[176:179], v[200:203], v[38:41]
	v_mfma_i32_16x16x64_i8 v[34:37], v[184:187], v[200:203], v[34:37]
	v_mfma_i32_16x16x64_i8 v[22:25], v[176:179], v[208:211], v[22:25]
	v_mfma_i32_16x16x64_i8 v[18:21], v[184:187], v[208:211], v[18:21]
	v_mfma_i32_16x16x64_i8 v[6:9], v[176:179], v[216:219], v[6:9]
	v_mfma_i32_16x16x64_i8 v[2:5], v[184:187], v[216:219], v[2:5]
	s_barrier
	s_add_i32 s38, 0, 0x18000
	s_add_i32 s39, 0, 0x1c000
	v_add_u32_e32 v134, s38, v167
	v_add_u32_e32 v154, s39, v167
	ds_read_b128 v[122:125], v134
	ds_read_b128 v[126:129], v134 offset:1024
	ds_read_b128 v[130:133], v134 offset:2048
	ds_read_b128 v[134:137], v134 offset:3072
	ds_read_b128 v[172:175], v154
	ds_read_b128 v[176:179], v154 offset:1024
	ds_read_b128 v[180:183], v154 offset:2048
	ds_read_b128 v[184:187], v154 offset:3072
	s_add_u32 s24, s24, 0x158000
	s_addc_u32 s25, s25, 0
	s_mov_b32 m0, s33
	ds_read_b128 v[188:191], v171 offset:32768
	ds_read_b128 v[192:195], v171 offset:33792
	ds_read_b128 v[196:199], v171 offset:34816
	ds_read_b128 v[200:203], v171 offset:35840
	ds_read_b128 v[204:207], v171 offset:36864
	ds_read_b128 v[208:211], v171 offset:37888
	ds_read_b128 v[212:215], v171 offset:38912
	ds_read_b128 v[216:219], v171 offset:39936
	global_load_lds_dwordx4 v146, s[24:25]
	s_mov_b32 m0, s34
	s_nop 0
	global_load_lds_dwordx4 v150, s[24:25]
	s_waitcnt vmcnt(8)
	s_waitcnt lgkmcnt(0)
	s_barrier
	v_mfma_i32_16x16x64_i8 v[142:145], v[122:125], v[188:191], v[142:145]
	v_mfma_i32_16x16x64_i8 v[138:141], v[130:133], v[188:191], v[138:141]
	v_mfma_i32_16x16x64_i8 v[110:113], v[122:125], v[196:199], v[110:113]
	v_mfma_i32_16x16x64_i8 v[106:109], v[130:133], v[196:199], v[106:109]
	v_mfma_i32_16x16x64_i8 v[94:97], v[122:125], v[204:207], v[94:97]
	v_mfma_i32_16x16x64_i8 v[90:93], v[130:133], v[204:207], v[90:93]
	v_mfma_i32_16x16x64_i8 v[78:81], v[122:125], v[212:215], v[78:81]
	v_mfma_i32_16x16x64_i8 v[74:77], v[130:133], v[212:215], v[74:77]
	v_mfma_i32_16x16x64_i8 v[142:145], v[126:129], v[192:195], v[142:145]
	v_mfma_i32_16x16x64_i8 v[138:141], v[134:137], v[192:195], v[138:141]
	v_mfma_i32_16x16x64_i8 v[110:113], v[126:129], v[200:203], v[110:113]
	v_mfma_i32_16x16x64_i8 v[106:109], v[134:137], v[200:203], v[106:109]
	v_mfma_i32_16x16x64_i8 v[94:97], v[126:129], v[208:211], v[94:97]
	v_mfma_i32_16x16x64_i8 v[90:93], v[134:137], v[208:211], v[90:93]
	v_mfma_i32_16x16x64_i8 v[78:81], v[126:129], v[216:219], v[78:81]
	v_mfma_i32_16x16x64_i8 v[74:77], v[134:137], v[216:219], v[74:77]
	v_mfma_i32_16x16x64_i8 v[118:121], v[172:175], v[188:191], v[118:121]
	v_mfma_i32_16x16x64_i8 v[114:117], v[180:183], v[188:191], v[114:117]
	v_mfma_i32_16x16x64_i8 v[102:105], v[172:175], v[196:199], v[102:105]
	v_mfma_i32_16x16x64_i8 v[98:101], v[180:183], v[196:199], v[98:101]
	v_mfma_i32_16x16x64_i8 v[86:89], v[172:175], v[204:207], v[86:89]
	v_mfma_i32_16x16x64_i8 v[82:85], v[180:183], v[204:207], v[82:85]
	v_mfma_i32_16x16x64_i8 v[70:73], v[172:175], v[212:215], v[70:73]
	v_mfma_i32_16x16x64_i8 v[66:69], v[180:183], v[212:215], v[66:69]
	v_mfma_i32_16x16x64_i8 v[118:121], v[176:179], v[192:195], v[118:121]
	v_mfma_i32_16x16x64_i8 v[114:117], v[184:187], v[192:195], v[114:117]
	v_mfma_i32_16x16x64_i8 v[102:105], v[176:179], v[200:203], v[102:105]
	v_mfma_i32_16x16x64_i8 v[98:101], v[184:187], v[200:203], v[98:101]
	v_mfma_i32_16x16x64_i8 v[86:89], v[176:179], v[208:211], v[86:89]
	v_mfma_i32_16x16x64_i8 v[82:85], v[184:187], v[208:211], v[82:85]
	v_mfma_i32_16x16x64_i8 v[70:73], v[176:179], v[216:219], v[70:73]
	v_mfma_i32_16x16x64_i8 v[66:69], v[184:187], v[216:219], v[66:69]
	s_barrier
	s_add_i32 s24, s38, s29
	s_mov_b32 m0, s24
	ds_read_b128 v[188:191], v171 offset:49152
	ds_read_b128 v[192:195], v171 offset:50176
	ds_read_b128 v[196:199], v171 offset:51200
	ds_read_b128 v[200:203], v171 offset:52224
	ds_read_b128 v[204:207], v171 offset:53248
	ds_read_b128 v[208:211], v171 offset:54272
	ds_read_b128 v[212:215], v171 offset:55296
	ds_read_b128 v[216:219], v171 offset:56320
	global_load_lds_dwordx4 v148, s[98:99]
	s_add_i32 m0, s24, 0x2000
	s_add_u32 s22, s22, 0x158080
	s_addc_u32 s23, s23, 0
	s_add_i32 s24, s39, s29
	global_load_lds_dwordx4 v152, s[98:99]
	s_mov_b32 m0, s24
	s_nop 0
	global_load_lds_dwordx4 v148, s[22:23]
	s_add_i32 m0, s24, 0x2000
	s_nop 0
	global_load_lds_dwordx4 v152, s[22:23]
	s_mov_b32 m0, s36
	s_nop 0
	global_load_lds_dwordx4 v146, s[100:101]
	s_mov_b32 m0, s37
	s_nop 0
	global_load_lds_dwordx4 v150, s[100:101]
	s_waitcnt vmcnt(8)
	s_waitcnt lgkmcnt(0)
	s_barrier
	v_mfma_i32_16x16x64_i8 v[62:65], v[122:125], v[188:191], v[62:65]
	v_mfma_i32_16x16x64_i8 v[58:61], v[130:133], v[188:191], v[58:61]
	v_mfma_i32_16x16x64_i8 v[46:49], v[122:125], v[196:199], v[46:49]
	v_mfma_i32_16x16x64_i8 v[42:45], v[130:133], v[196:199], v[42:45]
	v_mfma_i32_16x16x64_i8 v[30:33], v[122:125], v[204:207], v[30:33]
	v_mfma_i32_16x16x64_i8 v[26:29], v[130:133], v[204:207], v[26:29]
	v_mfma_i32_16x16x64_i8 v[14:17], v[122:125], v[212:215], v[14:17]
	v_mfma_i32_16x16x64_i8 v[10:13], v[130:133], v[212:215], v[10:13]
	v_mfma_i32_16x16x64_i8 v[62:65], v[126:129], v[192:195], v[62:65]
	v_mfma_i32_16x16x64_i8 v[58:61], v[134:137], v[192:195], v[58:61]
	v_mfma_i32_16x16x64_i8 v[46:49], v[126:129], v[200:203], v[46:49]
	v_mfma_i32_16x16x64_i8 v[42:45], v[134:137], v[200:203], v[42:45]
	v_mfma_i32_16x16x64_i8 v[30:33], v[126:129], v[208:211], v[30:33]
	v_mfma_i32_16x16x64_i8 v[26:29], v[134:137], v[208:211], v[26:29]
	v_mfma_i32_16x16x64_i8 v[14:17], v[126:129], v[216:219], v[14:17]
	v_mfma_i32_16x16x64_i8 v[10:13], v[134:137], v[216:219], v[10:13]
	v_mfma_i32_16x16x64_i8 v[54:57], v[172:175], v[188:191], v[54:57]
	v_mfma_i32_16x16x64_i8 v[50:53], v[180:183], v[188:191], v[50:53]
	v_mfma_i32_16x16x64_i8 v[38:41], v[172:175], v[196:199], v[38:41]
	v_mfma_i32_16x16x64_i8 v[34:37], v[180:183], v[196:199], v[34:37]
	v_mfma_i32_16x16x64_i8 v[22:25], v[172:175], v[204:207], v[22:25]
	v_mfma_i32_16x16x64_i8 v[18:21], v[180:183], v[204:207], v[18:21]
	v_mfma_i32_16x16x64_i8 v[6:9], v[172:175], v[212:215], v[6:9]
	v_mfma_i32_16x16x64_i8 v[2:5], v[180:183], v[212:215], v[2:5]
	v_mfma_i32_16x16x64_i8 v[54:57], v[176:179], v[192:195], v[54:57]
	v_mfma_i32_16x16x64_i8 v[50:53], v[184:187], v[192:195], v[50:53]
	v_mfma_i32_16x16x64_i8 v[38:41], v[176:179], v[200:203], v[38:41]
	v_mfma_i32_16x16x64_i8 v[34:37], v[184:187], v[200:203], v[34:37]
	v_mfma_i32_16x16x64_i8 v[22:25], v[176:179], v[208:211], v[22:25]
	v_mfma_i32_16x16x64_i8 v[18:21], v[184:187], v[208:211], v[18:21]
	v_mfma_i32_16x16x64_i8 v[6:9], v[176:179], v[216:219], v[6:9]
	v_mfma_i32_16x16x64_i8 v[2:5], v[184:187], v[216:219], v[2:5]
	s_barrier
	s_add_i32 s49, s49, 2
	s_add_u32 s20, s20, 0x100
	s_addc_u32 s21, s21, 0
	s_add_u32 s47, s47, 0x100
	s_addc_u32 s48, s48, 0
	s_cmpk_gt_u32 s49, 0x53
	s_cbranch_scc0 .LBB0_1899
	s_setprio 0
	s_and_b64 vcc, exec, s[16:17]
	s_cbranch_vccz .LBB0_1902
	s_barrier
